# speedup vs baseline: 1.0102x; 1.0102x over previous
.LBB5_6:
	s_or_b64 exec, exec, s[10:11]
	s_load_dwordx2 s[10:11], s[0:1], 0x80
	s_load_dwordx2 s[36:37], s[0:1], 0x70
	s_load_dwordx2 s[40:41], s[0:1], 0x60
	s_load_dwordx4 s[20:23], s[0:1], 0x50
	s_load_dwordx8 s[12:19], s[0:1], 0x30
	s_load_dwordx4 s[24:27], s[0:1], 0x10
	s_load_dwordx2 s[46:47], s[0:1], 0x20
	s_and_b32 s58, s59, 1
	s_cmp_eq_u32 s35, 0
	s_cselect_b32 s42, s3, s7
	s_ashr_i32 s7, s6, 31
	s_lshl_b64 s[52:53], s[6:7], 22
	s_waitcnt lgkmcnt(0)
	s_lshl_b32 s64, s42, 11
	s_lshl_b32 s65, s58, 10
	s_add_u32 s64, s64, s65
	s_add_u32 s66, s24, s64
	s_addc_u32 s67, s25, 0
	s_mov_b32 m0, 0x22240
	v_and_b32_e32 v254, 63, v0
	v_lshlrev_b32_e32 v254, 4, v254
	global_load_lds_dwordx4 v254, s[66:67]
	s_lshl_b32 s64, s42, 10
	s_add_u32 s66, s12, s64
	s_addc_u32 s67, s13, 0
	s_mov_b32 m0, 0x22640
	s_lshl_b32 s65, s42, 2
	global_load_lds_dwordx4 v254, s[66:67]
	s_add_u32 s66, s14, s64
	s_addc_u32 s67, s15, 0
	s_mov_b32 m0, 0x22a40
	s_nop 0
	global_load_lds_dwordx4 v254, s[66:67]
	s_add_u32 s66, s16, s64
	s_addc_u32 s67, s17, 0
	s_mov_b32 m0, 0x22e40
	s_load_dword s69, s[18:19], s65
	global_load_lds_dwordx4 v254, s[66:67]
	s_add_u32 s3, s28, s52
	s_addc_u32 s7, s29, s53
	s_lshl_b32 s35, s33, 19
	s_and_b32 s35, s35, 0x300000
	s_add_u32 s50, s3, s35
	s_addc_u32 s51, s7, 0
	s_ashr_i32 s43, s42, 31
	s_lshl_b32 s7, s58, 8
	s_lshl_b64 s[54:55], s[42:43], 21
	v_lshlrev_b32_e32 v162, 4, v0
	v_and_b32_e32 v2, 32, v0
	s_add_u32 s35, s30, s54
	v_bitop3_b32 v12, v162, v2, 48 bitop3:0x6c
	v_and_b32_e32 v13, 64, v0
	s_addc_u32 s38, s31, s55
	s_lshl_b32 s3, s58, 20
	v_lshrrev_b32_e32 v4, 3, v0
	v_bfe_u32 v3, v0, 2, 4
	v_or_b32_e32 v2, v12, v13
	v_or_b32_e32 v164, 0x2000, v162
	s_add_u32 s56, s35, s3
	v_and_or_b32 v4, v4, 48, v3
	v_lshrrev_b32_e32 v2, 1, v2
	v_lshrrev_b32_e32 v5, 7, v164
	s_movk_i32 s35, 0x70
	v_add_u32_e32 v142, 0, v162
	v_lshl_or_b32 v4, v4, 11, v2
	v_and_or_b32 v5, v5, s35, v3
	v_readfirstlane_b32 s35, v142
	v_add_u32_e32 v143, 0x2000, v142
	v_lshlrev_b32_e32 v130, 1, v4
	s_mov_b32 m0, s35
	v_readfirstlane_b32 s35, v143
	s_addc_u32 s57, s38, 0
	global_load_lds_dwordx4 v130, s[50:51]
	s_mov_b32 m0, s35
	s_add_i32 s35, 0, 0x10000
	v_lshl_or_b32 v2, v5, 11, v2
	v_add_u32_e32 v144, s35, v162
	v_lshlrev_b32_e32 v132, 1, v2
	v_readfirstlane_b32 s38, v144
	v_add_u32_e32 v145, 0x2000, v144
	global_load_lds_dwordx4 v132, s[50:51]
	s_mov_b32 m0, s38
	v_readfirstlane_b32 s38, v145
	v_add_u32_e32 v151, 0x4000, v142
	global_load_lds_dwordx4 v130, s[56:57]
	s_mov_b32 m0, s38
	s_add_u32 s38, s50, 0x80000
	v_readfirstlane_b32 s44, v151
	v_add_u32_e32 v153, 0x6000, v142
	global_load_lds_dwordx4 v132, s[56:57]
	s_addc_u32 s39, s51, 0
	s_mov_b32 m0, s44
	v_readfirstlane_b32 s44, v153
	global_load_lds_dwordx4 v130, s[38:39]
	s_mov_b32 m0, s44
	v_mov_b32_e32 v2, 0
	global_load_lds_dwordx4 v132, s[38:39]
	s_add_u32 s38, s56, 0x80000
	s_addc_u32 s39, s57, 0
	s_add_i32 s60, 0, 0x14000
	v_add_u32_e32 v154, s60, v162
	v_add_u32_e32 v155, 0x2000, v154
	v_readfirstlane_b32 s44, v154
	s_mov_b32 m0, s44
	v_readfirstlane_b32 s44, v155
	global_load_lds_dwordx4 v130, s[38:39]
	s_mov_b32 m0, s44
	v_lshrrev_b32_e32 v14, 8, v0
	global_load_lds_dwordx4 v132, s[38:39]
	v_mov_b32_e32 v131, v2
	v_mov_b32_e32 v133, v2
	v_lshl_add_u64 v[10:11], s[50:51], 0, v[130:131]
	v_lshl_add_u64 v[8:9], s[50:51], 0, v[132:133]
	v_lshl_add_u64 v[6:7], s[56:57], 0, v[130:131]
	v_lshl_add_u64 v[4:5], s[56:57], 0, v[132:133]
	v_cmp_eq_u32_e32 vcc, 1, v14
	s_and_saveexec_b64 s[38:39], vcc
	s_cbranch_execz .LBB5_8
	s_barrier

.LBB5_12:
	s_or_b64 exec, exec, s[0:1]
	s_lshl_b32 s0, s42, 9
	s_ashr_i32 s1, s0, 31
	s_lshl_b64 s[0:1], s[0:1], 2
	s_add_u32 s0, s24, s0
	s_addc_u32 s1, s25, s1
	s_lshl_b32 s2, s7, 2
	v_bfe_u32 v153, v0, 6, 2
	s_add_u32 s0, s0, s2
	s_addc_u32 s1, s1, 0
	v_lshlrev_b32_e32 v148, 7, v153
	v_mov_b32_e32 v149, 0
	v_lshl_add_u64 v[10:11], s[0:1], 0, v[148:149]
	v_mov_b32_e32 v147, v149
	v_lshl_add_u64 v[10:11], v[10:11], 0, v[146:147]
	v_and_b32_e32 v254, 48, v0
	v_lshl_add_u32 v254, v153, 7, v254
	v_add_u32_e32 v254, 0x22240, v254
	ds_read_b128 v[34:37], v254
	ds_read_b128 v[26:29], v254 offset:64
	ds_read_b128 v[18:21], v254 offset:512
	ds_read_b128 v[10:13], v254 offset:576
	s_ashr_i32 s35, s34, 31
	s_and_b32 s50, s59, 6
	s_lshl_b64 s[2:3], s[34:35], 3
	s_or_b32 s7, s2, s50
	s_or_b32 s2, s7, s58
	s_lshl_b64 s[24:25], s[2:3], 16
	v_lshrrev_b32_e32 v187, 6, v0
	s_add_u32 s28, s26, s24
	v_and_b32_e32 v157, 4, v187
	s_addc_u32 s29, s27, s25
	s_lshl_b32 s2, s58, 3
	v_lshlrev_b32_e32 v147, 6, v188
	v_lshrrev_b32_e32 v148, 1, v0
	v_lshlrev_b32_e32 v154, 10, v153
	v_lshlrev_b32_e32 v158, 13, v157
	s_cmp_lg_u32 s58, 0
	v_lshl_or_b32 v159, v157, 4, s2
	v_and_or_b32 v155, v148, 24, v147
	v_or_b32_e32 v148, v154, v158
	s_cselect_b64 s[24:25], -1, 0
	v_or_b32_e32 v156, v153, v159
	s_mov_b64 s[0:1], -1
	v_lshl_add_u64 v[150:151], s[28:29], 0, v[148:149]
	v_or_b32_e32 v148, v155, v152
	v_lshl_add_u32 v156, v156, 10, 0
	s_and_b64 vcc, exec, s[24:25]
	s_waitcnt vmcnt(0) lgkmcnt(0)
	s_barrier
	v_fmamk_f32 v142, v142, 0x3c800000, v34
	v_fmamk_f32 v143, v143, 0x3c800000, v35
	v_fmamk_f32 v144, v144, 0x3c800000, v36
	v_fmamk_f32 v145, v145, 0x3c800000, v37
	v_max_f32_e32 v142, 0, v142
	v_max_f32_e32 v160, 0, v143
	v_max_f32_e32 v143, 0, v144
	v_max_f32_e32 v144, 0, v145
	v_cvt_pk_f16_f32 v143, v143, v144
	v_cvt_pk_f16_f32 v142, v142, v160
	s_cbranch_vccz .LBB5_14
	v_lshl_add_u64 v[144:145], v[150:151], 0, v[148:149]
	global_store_dwordx2 v[144:145], v[142:143], off sc1
	s_mov_b64 s[0:1], 0

.LBB5_148:
	s_or_b32 s2, s49, s28
	s_lshl_b32 s0, s2, 12
	s_mov_b32 s1, 0
	v_lshl_add_u64 v[176:177], v[166:167], 0, s[0:1]
	s_waitcnt vmcnt(0)
	s_waitcnt vmcnt(0) lgkmcnt(0)
	s_barrier
	global_load_dwordx4 v[162:165], v[176:177], off
	global_load_dwordx4 v[168:171], v[176:177], off offset:1024
	global_load_dwordx4 v[172:175], v[176:177], off offset:2048
	s_nop 0
	global_load_dwordx4 v[176:179], v[176:177], off offset:3072
	v_lshl_add_u32 v208, s51, 10, v191
	ds_read_b128 v[192:195], v208
	ds_read_b128 v[196:199], v208 offset:16384
	ds_read_b128 v[200:203], v208 offset:32768
	ds_read_b128 v[204:207], v208 offset:49152
	s_setprio 1
	s_waitcnt lgkmcnt(3)
	v_mfma_f32_16x16x32_f16 v[34:37], v[2:5], v[192:195], v[34:37]
	v_mfma_f32_16x16x32_f16 v[38:41], v[6:9], v[192:195], v[38:41]
	v_mfma_f32_16x16x32_f16 v[42:45], v[10:13], v[192:195], v[42:45]
	v_mfma_f32_16x16x32_f16 v[46:49], v[14:17], v[192:195], v[46:49]
	s_waitcnt lgkmcnt(2)
	v_mfma_f32_16x16x32_f16 v[50:53], v[2:5], v[196:199], v[50:53]
	v_mfma_f32_16x16x32_f16 v[54:57], v[6:9], v[196:199], v[54:57]
	v_mfma_f32_16x16x32_f16 v[58:61], v[10:13], v[196:199], v[58:61]
	v_mfma_f32_16x16x32_f16 v[62:65], v[14:17], v[196:199], v[62:65]
	s_waitcnt lgkmcnt(1)
	v_mfma_f32_16x16x32_f16 v[66:69], v[2:5], v[200:203], v[66:69]
	v_mfma_f32_16x16x32_f16 v[70:73], v[6:9], v[200:203], v[70:73]
	v_mfma_f32_16x16x32_f16 v[74:77], v[10:13], v[200:203], v[74:77]
	v_mfma_f32_16x16x32_f16 v[78:81], v[14:17], v[200:203], v[78:81]
	s_waitcnt lgkmcnt(0)
	v_mfma_f32_16x16x32_f16 v[82:85], v[2:5], v[204:207], v[82:85]
	v_mfma_f32_16x16x32_f16 v[86:89], v[6:9], v[204:207], v[86:89]
	v_mfma_f32_16x16x32_f16 v[90:93], v[10:13], v[204:207], v[90:93]
	v_mfma_f32_16x16x32_f16 v[94:97], v[14:17], v[204:207], v[94:97]
	s_setprio 0
	v_add_u32_e32 v192, 0x10000, v208
	v_add_u32_e32 v196, 0x14000, v208
	v_add_u32_e32 v200, 0x18000, v208
	v_add_u32_e32 v204, 0x1c000, v208
	ds_read_b128 v[192:195], v192
	ds_read_b128 v[196:199], v196
	ds_read_b128 v[200:203], v200
	ds_read_b128 v[204:207], v204
	s_setprio 1
	s_waitcnt lgkmcnt(3)
	v_mfma_f32_16x16x32_f16 v[98:101], v[2:5], v[192:195], v[98:101]
	v_mfma_f32_16x16x32_f16 v[102:105], v[6:9], v[192:195], v[102:105]
	v_mfma_f32_16x16x32_f16 v[106:109], v[10:13], v[192:195], v[106:109]
	v_mfma_f32_16x16x32_f16 v[110:113], v[14:17], v[192:195], v[110:113]
	s_waitcnt lgkmcnt(2)
	v_mfma_f32_16x16x32_f16 v[114:117], v[2:5], v[196:199], v[114:117]
	v_mfma_f32_16x16x32_f16 v[118:121], v[6:9], v[196:199], v[118:121]
	v_mfma_f32_16x16x32_f16 v[122:125], v[10:13], v[196:199], v[122:125]
	v_mfma_f32_16x16x32_f16 v[126:129], v[14:17], v[196:199], v[126:129]
	s_waitcnt lgkmcnt(1)
	v_mfma_f32_16x16x32_f16 v[130:133], v[2:5], v[200:203], v[130:133]
	v_mfma_f32_16x16x32_f16 v[134:137], v[6:9], v[200:203], v[134:137]
	v_mfma_f32_16x16x32_f16 v[138:141], v[10:13], v[200:203], v[138:141]
	v_mfma_f32_16x16x32_f16 v[142:145], v[14:17], v[200:203], v[142:145]
	s_waitcnt lgkmcnt(0)
	v_mfma_f32_16x16x32_f16 v[2:5], v[2:5], v[204:207], v[146:149]
	v_mfma_f32_16x16x32_f16 v[6:9], v[6:9], v[204:207], v[150:153]
	v_mfma_f32_16x16x32_f16 v[10:13], v[10:13], v[204:207], v[154:157]
	v_mfma_f32_16x16x32_f16 v[14:17], v[14:17], v[204:207], v[158:161]
	s_setprio 0
	s_or_b32 s3, s49, s29
	s_lshl_b32 s0, s3, 12
	v_lshl_add_u64 v[158:159], v[166:167], 0, s[0:1]
	global_load_dwordx4 v[146:149], v[158:159], off
	global_load_dwordx4 v[150:153], v[158:159], off offset:1024
	global_load_dwordx4 v[154:157], v[158:159], off offset:2048
	s_nop 0
	global_load_dwordx4 v[158:161], v[158:159], off offset:3072
	v_lshl_add_u32 v208, s52, 10, v191
	ds_read_b128 v[192:195], v208
	ds_read_b128 v[196:199], v208 offset:16384
	ds_read_b128 v[200:203], v208 offset:32768
	ds_read_b128 v[204:207], v208 offset:49152
	s_setprio 1
	s_waitcnt lgkmcnt(3)
	v_mfma_f32_16x16x32_f16 v[34:37], v[18:21], v[192:195], v[34:37]
	v_mfma_f32_16x16x32_f16 v[38:41], v[22:25], v[192:195], v[38:41]
	v_mfma_f32_16x16x32_f16 v[42:45], v[26:29], v[192:195], v[42:45]
	v_mfma_f32_16x16x32_f16 v[46:49], v[30:33], v[192:195], v[46:49]
	s_waitcnt lgkmcnt(2)
	v_mfma_f32_16x16x32_f16 v[50:53], v[18:21], v[196:199], v[50:53]
	v_mfma_f32_16x16x32_f16 v[54:57], v[22:25], v[196:199], v[54:57]
	v_mfma_f32_16x16x32_f16 v[58:61], v[26:29], v[196:199], v[58:61]
	v_mfma_f32_16x16x32_f16 v[62:65], v[30:33], v[196:199], v[62:65]
	s_waitcnt lgkmcnt(1)
	v_mfma_f32_16x16x32_f16 v[66:69], v[18:21], v[200:203], v[66:69]
	v_mfma_f32_16x16x32_f16 v[70:73], v[22:25], v[200:203], v[70:73]
	v_mfma_f32_16x16x32_f16 v[74:77], v[26:29], v[200:203], v[74:77]
	v_mfma_f32_16x16x32_f16 v[78:81], v[30:33], v[200:203], v[78:81]
	s_waitcnt lgkmcnt(0)
	v_mfma_f32_16x16x32_f16 v[82:85], v[18:21], v[204:207], v[82:85]
	v_mfma_f32_16x16x32_f16 v[86:89], v[22:25], v[204:207], v[86:89]
	v_mfma_f32_16x16x32_f16 v[90:93], v[26:29], v[204:207], v[90:93]
	v_mfma_f32_16x16x32_f16 v[94:97], v[30:33], v[204:207], v[94:97]
	s_setprio 0
	v_add_u32_e32 v192, 0x10000, v208
	v_add_u32_e32 v196, 0x14000, v208
	v_add_u32_e32 v200, 0x18000, v208
	v_add_u32_e32 v204, 0x1c000, v208
	ds_read_b128 v[192:195], v192
	ds_read_b128 v[196:199], v196
	ds_read_b128 v[200:203], v200
	ds_read_b128 v[204:207], v204
	s_setprio 1
	s_waitcnt lgkmcnt(3)
	v_mfma_f32_16x16x32_f16 v[98:101], v[18:21], v[192:195], v[98:101]
	v_mfma_f32_16x16x32_f16 v[102:105], v[22:25], v[192:195], v[102:105]
	v_mfma_f32_16x16x32_f16 v[106:109], v[26:29], v[192:195], v[106:109]
	v_mfma_f32_16x16x32_f16 v[110:113], v[30:33], v[192:195], v[110:113]
	s_waitcnt lgkmcnt(2)
	v_mfma_f32_16x16x32_f16 v[114:117], v[18:21], v[196:199], v[114:117]
	v_mfma_f32_16x16x32_f16 v[118:121], v[22:25], v[196:199], v[118:121]
	v_mfma_f32_16x16x32_f16 v[122:125], v[26:29], v[196:199], v[122:125]
	v_mfma_f32_16x16x32_f16 v[126:129], v[30:33], v[196:199], v[126:129]
	s_waitcnt lgkmcnt(1)
	v_mfma_f32_16x16x32_f16 v[130:133], v[18:21], v[200:203], v[130:133]
	v_mfma_f32_16x16x32_f16 v[134:137], v[22:25], v[200:203], v[134:137]
	v_mfma_f32_16x16x32_f16 v[138:141], v[26:29], v[200:203], v[138:141]
	s_waitcnt lgkmcnt(0)
	v_mfma_f32_16x16x32_f16 v[2:5], v[18:21], v[204:207], v[2:5]
	v_mfma_f32_16x16x32_f16 v[6:9], v[22:25], v[204:207], v[6:9]
	v_mfma_f32_16x16x32_f16 v[10:13], v[26:29], v[204:207], v[10:13]
	v_mfma_f32_16x16x32_f16 v[14:17], v[30:33], v[204:207], v[14:17]
	v_mfma_f32_16x16x32_f16 v[142:145], v[30:33], v[200:203], v[142:145]
	s_setprio 0
	s_xor_b32 s7, s51, 4
	s_lshl_b32 s0, s7, 12
	v_lshl_add_u64 v[30:31], v[166:167], 0, s[0:1]
	global_load_dwordx4 v[18:21], v[30:31], off
	global_load_dwordx4 v[22:25], v[30:31], off offset:1024
	global_load_dwordx4 v[26:29], v[30:31], off offset:2048
	s_nop 0
	global_load_dwordx4 v[30:33], v[30:31], off offset:3072
	v_lshl_add_u32 v208, s2, 10, v191
	ds_read_b128 v[192:195], v208
	ds_read_b128 v[196:199], v208 offset:16384
	ds_read_b128 v[200:203], v208 offset:32768
	ds_read_b128 v[204:207], v208 offset:49152
	s_setprio 1
	s_waitcnt vmcnt(11) lgkmcnt(3)
	v_mfma_f32_16x16x32_f16 v[34:37], v[162:165], v[192:195], v[34:37]
	s_waitcnt vmcnt(10)
	v_mfma_f32_16x16x32_f16 v[38:41], v[168:171], v[192:195], v[38:41]
	s_waitcnt vmcnt(9)
	v_mfma_f32_16x16x32_f16 v[42:45], v[172:175], v[192:195], v[42:45]
	s_waitcnt vmcnt(8)
	v_mfma_f32_16x16x32_f16 v[46:49], v[176:179], v[192:195], v[46:49]
	s_waitcnt lgkmcnt(2)
	v_mfma_f32_16x16x32_f16 v[50:53], v[162:165], v[196:199], v[50:53]
	v_mfma_f32_16x16x32_f16 v[54:57], v[168:171], v[196:199], v[54:57]
	v_mfma_f32_16x16x32_f16 v[58:61], v[172:175], v[196:199], v[58:61]
	v_mfma_f32_16x16x32_f16 v[62:65], v[176:179], v[196:199], v[62:65]
	s_waitcnt lgkmcnt(1)
	v_mfma_f32_16x16x32_f16 v[66:69], v[162:165], v[200:203], v[66:69]
	v_mfma_f32_16x16x32_f16 v[70:73], v[168:171], v[200:203], v[70:73]
	v_mfma_f32_16x16x32_f16 v[74:77], v[172:175], v[200:203], v[74:77]
	v_mfma_f32_16x16x32_f16 v[78:81], v[176:179], v[200:203], v[78:81]
	s_waitcnt lgkmcnt(0)
	v_mfma_f32_16x16x32_f16 v[82:85], v[162:165], v[204:207], v[82:85]
	v_mfma_f32_16x16x32_f16 v[86:89], v[168:171], v[204:207], v[86:89]
	v_mfma_f32_16x16x32_f16 v[90:93], v[172:175], v[204:207], v[90:93]
	v_mfma_f32_16x16x32_f16 v[94:97], v[176:179], v[204:207], v[94:97]
	s_setprio 0
	v_add_u32_e32 v192, 0x10000, v208
	v_add_u32_e32 v196, 0x14000, v208
	v_add_u32_e32 v200, 0x18000, v208
	v_add_u32_e32 v204, 0x1c000, v208
	ds_read_b128 v[192:195], v192
	ds_read_b128 v[196:199], v196
	ds_read_b128 v[200:203], v200
	ds_read_b128 v[204:207], v204
	s_setprio 1
	s_waitcnt lgkmcnt(3)
	v_mfma_f32_16x16x32_f16 v[98:101], v[162:165], v[192:195], v[98:101]
	v_mfma_f32_16x16x32_f16 v[102:105], v[168:171], v[192:195], v[102:105]
	v_mfma_f32_16x16x32_f16 v[106:109], v[172:175], v[192:195], v[106:109]
	v_mfma_f32_16x16x32_f16 v[110:113], v[176:179], v[192:195], v[110:113]
	s_waitcnt lgkmcnt(2)
	v_mfma_f32_16x16x32_f16 v[114:117], v[162:165], v[196:199], v[114:117]
	v_mfma_f32_16x16x32_f16 v[118:121], v[168:171], v[196:199], v[118:121]
	v_mfma_f32_16x16x32_f16 v[122:125], v[172:175], v[196:199], v[122:125]
	v_mfma_f32_16x16x32_f16 v[126:129], v[176:179], v[196:199], v[126:129]
	s_waitcnt lgkmcnt(1)
	v_mfma_f32_16x16x32_f16 v[130:133], v[162:165], v[200:203], v[130:133]
	v_mfma_f32_16x16x32_f16 v[134:137], v[168:171], v[200:203], v[134:137]
	v_mfma_f32_16x16x32_f16 v[138:141], v[172:175], v[200:203], v[138:141]
	s_waitcnt lgkmcnt(0)
	v_mfma_f32_16x16x32_f16 v[2:5], v[162:165], v[204:207], v[2:5]
	v_mfma_f32_16x16x32_f16 v[6:9], v[168:171], v[204:207], v[6:9]
	v_mfma_f32_16x16x32_f16 v[10:13], v[172:175], v[204:207], v[10:13]
	v_mfma_f32_16x16x32_f16 v[14:17], v[176:179], v[204:207], v[14:17]
	v_mfma_f32_16x16x32_f16 v[142:145], v[176:179], v[200:203], v[142:145]
	s_setprio 0
	s_or_b32 s2, s49, s30
	s_lshl_b32 s0, s2, 12
	v_lshl_add_u64 v[176:177], v[166:167], 0, s[0:1]
	global_load_dwordx4 v[162:165], v[176:177], off
	global_load_dwordx4 v[168:171], v[176:177], off offset:1024
	global_load_dwordx4 v[172:175], v[176:177], off offset:2048
	s_nop 0
	global_load_dwordx4 v[176:179], v[176:177], off offset:3072
	v_lshl_add_u32 v208, s3, 10, v191
	ds_read_b128 v[192:195], v208
	ds_read_b128 v[196:199], v208 offset:16384
	ds_read_b128 v[200:203], v208 offset:32768
	ds_read_b128 v[204:207], v208 offset:49152
	s_setprio 1
	s_waitcnt vmcnt(11) lgkmcnt(3)
	v_mfma_f32_16x16x32_f16 v[34:37], v[146:149], v[192:195], v[34:37]
	s_waitcnt vmcnt(10)
	v_mfma_f32_16x16x32_f16 v[38:41], v[150:153], v[192:195], v[38:41]
	s_waitcnt vmcnt(9)
	v_mfma_f32_16x16x32_f16 v[42:45], v[154:157], v[192:195], v[42:45]
	s_waitcnt vmcnt(8)
	v_mfma_f32_16x16x32_f16 v[46:49], v[158:161], v[192:195], v[46:49]
	s_waitcnt lgkmcnt(2)
	v_mfma_f32_16x16x32_f16 v[50:53], v[146:149], v[196:199], v[50:53]
	v_mfma_f32_16x16x32_f16 v[54:57], v[150:153], v[196:199], v[54:57]
	v_mfma_f32_16x16x32_f16 v[58:61], v[154:157], v[196:199], v[58:61]
	v_mfma_f32_16x16x32_f16 v[62:65], v[158:161], v[196:199], v[62:65]
	s_waitcnt lgkmcnt(1)
	v_mfma_f32_16x16x32_f16 v[66:69], v[146:149], v[200:203], v[66:69]
	v_mfma_f32_16x16x32_f16 v[70:73], v[150:153], v[200:203], v[70:73]
	v_mfma_f32_16x16x32_f16 v[74:77], v[154:157], v[200:203], v[74:77]
	v_mfma_f32_16x16x32_f16 v[78:81], v[158:161], v[200:203], v[78:81]
	s_waitcnt lgkmcnt(0)
	v_mfma_f32_16x16x32_f16 v[82:85], v[146:149], v[204:207], v[82:85]
	v_mfma_f32_16x16x32_f16 v[86:89], v[150:153], v[204:207], v[86:89]
	v_mfma_f32_16x16x32_f16 v[90:93], v[154:157], v[204:207], v[90:93]
	v_mfma_f32_16x16x32_f16 v[94:97], v[158:161], v[204:207], v[94:97]
	s_setprio 0
	v_add_u32_e32 v192, 0x10000, v208
	v_add_u32_e32 v196, 0x14000, v208
	v_add_u32_e32 v200, 0x18000, v208
	v_add_u32_e32 v204, 0x1c000, v208
	ds_read_b128 v[192:195], v192
	ds_read_b128 v[196:199], v196
	ds_read_b128 v[200:203], v200
	ds_read_b128 v[204:207], v204
	s_setprio 1
	s_waitcnt lgkmcnt(3)
	v_mfma_f32_16x16x32_f16 v[98:101], v[146:149], v[192:195], v[98:101]
	v_mfma_f32_16x16x32_f16 v[102:105], v[150:153], v[192:195], v[102:105]
	v_mfma_f32_16x16x32_f16 v[106:109], v[154:157], v[192:195], v[106:109]
	v_mfma_f32_16x16x32_f16 v[110:113], v[158:161], v[192:195], v[110:113]
	s_waitcnt lgkmcnt(2)
	v_mfma_f32_16x16x32_f16 v[114:117], v[146:149], v[196:199], v[114:117]
	v_mfma_f32_16x16x32_f16 v[118:121], v[150:153], v[196:199], v[118:121]
	v_mfma_f32_16x16x32_f16 v[122:125], v[154:157], v[196:199], v[122:125]
	v_mfma_f32_16x16x32_f16 v[126:129], v[158:161], v[196:199], v[126:129]
	s_waitcnt lgkmcnt(1)
	v_mfma_f32_16x16x32_f16 v[130:133], v[146:149], v[200:203], v[130:133]
	v_mfma_f32_16x16x32_f16 v[134:137], v[150:153], v[200:203], v[134:137]
	v_mfma_f32_16x16x32_f16 v[138:141], v[154:157], v[200:203], v[138:141]
	s_waitcnt lgkmcnt(0)
	v_mfma_f32_16x16x32_f16 v[2:5], v[146:149], v[204:207], v[2:5]
	v_mfma_f32_16x16x32_f16 v[6:9], v[150:153], v[204:207], v[6:9]
	v_mfma_f32_16x16x32_f16 v[10:13], v[154:157], v[204:207], v[10:13]
	v_mfma_f32_16x16x32_f16 v[14:17], v[158:161], v[204:207], v[14:17]
	v_mfma_f32_16x16x32_f16 v[142:145], v[158:161], v[200:203], v[142:145]
	s_setprio 0
	s_or_b32 s3, s49, s31
	s_lshl_b32 s0, s3, 12
	v_lshl_add_u64 v[158:159], v[166:167], 0, s[0:1]
	global_load_dwordx4 v[146:149], v[158:159], off
	global_load_dwordx4 v[150:153], v[158:159], off offset:1024
	global_load_dwordx4 v[154:157], v[158:159], off offset:2048
	s_nop 0
	global_load_dwordx4 v[158:161], v[158:159], off offset:3072
	v_lshl_add_u32 v208, s7, 10, v191
	ds_read_b128 v[192:195], v208
	ds_read_b128 v[196:199], v208 offset:16384
	ds_read_b128 v[200:203], v208 offset:32768
	ds_read_b128 v[204:207], v208 offset:49152
	s_setprio 1
	s_waitcnt vmcnt(11) lgkmcnt(3)
	v_mfma_f32_16x16x32_f16 v[34:37], v[18:21], v[192:195], v[34:37]
	s_waitcnt vmcnt(10)
	v_mfma_f32_16x16x32_f16 v[38:41], v[22:25], v[192:195], v[38:41]
	s_waitcnt vmcnt(9)
	v_mfma_f32_16x16x32_f16 v[42:45], v[26:29], v[192:195], v[42:45]
	s_waitcnt vmcnt(8)
	v_mfma_f32_16x16x32_f16 v[46:49], v[30:33], v[192:195], v[46:49]
	s_waitcnt lgkmcnt(2)
	v_mfma_f32_16x16x32_f16 v[50:53], v[18:21], v[196:199], v[50:53]
	v_mfma_f32_16x16x32_f16 v[54:57], v[22:25], v[196:199], v[54:57]
	v_mfma_f32_16x16x32_f16 v[58:61], v[26:29], v[196:199], v[58:61]
	v_mfma_f32_16x16x32_f16 v[62:65], v[30:33], v[196:199], v[62:65]
	s_waitcnt lgkmcnt(1)
	v_mfma_f32_16x16x32_f16 v[66:69], v[18:21], v[200:203], v[66:69]
	v_mfma_f32_16x16x32_f16 v[70:73], v[22:25], v[200:203], v[70:73]
	v_mfma_f32_16x16x32_f16 v[74:77], v[26:29], v[200:203], v[74:77]
	v_mfma_f32_16x16x32_f16 v[78:81], v[30:33], v[200:203], v[78:81]
	s_waitcnt lgkmcnt(0)
	v_mfma_f32_16x16x32_f16 v[82:85], v[18:21], v[204:207], v[82:85]
	v_mfma_f32_16x16x32_f16 v[86:89], v[22:25], v[204:207], v[86:89]
	v_mfma_f32_16x16x32_f16 v[90:93], v[26:29], v[204:207], v[90:93]
	v_mfma_f32_16x16x32_f16 v[94:97], v[30:33], v[204:207], v[94:97]
	s_setprio 0
	v_add_u32_e32 v192, 0x10000, v208
	v_add_u32_e32 v196, 0x14000, v208
	v_add_u32_e32 v200, 0x18000, v208
	v_add_u32_e32 v204, 0x1c000, v208
	ds_read_b128 v[192:195], v192
	ds_read_b128 v[196:199], v196
	ds_read_b128 v[200:203], v200
	ds_read_b128 v[204:207], v204
	s_setprio 1
	s_waitcnt lgkmcnt(3)
	v_mfma_f32_16x16x32_f16 v[98:101], v[18:21], v[192:195], v[98:101]
	v_mfma_f32_16x16x32_f16 v[102:105], v[22:25], v[192:195], v[102:105]
	v_mfma_f32_16x16x32_f16 v[106:109], v[26:29], v[192:195], v[106:109]
	v_mfma_f32_16x16x32_f16 v[110:113], v[30:33], v[192:195], v[110:113]
	s_waitcnt lgkmcnt(2)
	v_mfma_f32_16x16x32_f16 v[114:117], v[18:21], v[196:199], v[114:117]
	v_mfma_f32_16x16x32_f16 v[118:121], v[22:25], v[196:199], v[118:121]
	v_mfma_f32_16x16x32_f16 v[122:125], v[26:29], v[196:199], v[122:125]
	v_mfma_f32_16x16x32_f16 v[126:129], v[30:33], v[196:199], v[126:129]
	s_waitcnt lgkmcnt(1)
	v_mfma_f32_16x16x32_f16 v[130:133], v[18:21], v[200:203], v[130:133]
	v_mfma_f32_16x16x32_f16 v[134:137], v[22:25], v[200:203], v[134:137]
	v_mfma_f32_16x16x32_f16 v[138:141], v[26:29], v[200:203], v[138:141]
	s_waitcnt lgkmcnt(0)
	v_mfma_f32_16x16x32_f16 v[2:5], v[18:21], v[204:207], v[2:5]
	v_mfma_f32_16x16x32_f16 v[6:9], v[22:25], v[204:207], v[6:9]
	v_mfma_f32_16x16x32_f16 v[10:13], v[26:29], v[204:207], v[10:13]
	v_mfma_f32_16x16x32_f16 v[14:17], v[30:33], v[204:207], v[14:17]
	v_mfma_f32_16x16x32_f16 v[142:145], v[30:33], v[200:203], v[142:145]
	s_setprio 0
	s_or_b32 s7, s49, s48
	s_lshl_b32 s0, s7, 12
	v_lshl_add_u64 v[26:27], v[166:167], 0, s[0:1]
	global_load_dwordx4 v[18:21], v[26:27], off
	global_load_dwordx4 v[22:25], v[26:27], off offset:1024
	global_load_dwordx4 v[30:33], v[26:27], off offset:2048
	global_load_dwordx4 v[192:195], v[26:27], off offset:3072
	v_lshl_add_u32 v166, s2, 10, v191
	ds_read_b128 v[26:29], v166
	ds_read_b128 v[196:199], v166 offset:16384
	ds_read_b128 v[200:203], v166 offset:32768
	ds_read_b128 v[204:207], v166 offset:49152
	s_setprio 1
	s_waitcnt vmcnt(11) lgkmcnt(3)
	v_mfma_f32_16x16x32_f16 v[34:37], v[162:165], v[26:29], v[34:37]
	s_waitcnt vmcnt(10)
	v_mfma_f32_16x16x32_f16 v[38:41], v[168:171], v[26:29], v[38:41]
	s_waitcnt vmcnt(9)
	v_mfma_f32_16x16x32_f16 v[42:45], v[172:175], v[26:29], v[42:45]
	s_waitcnt vmcnt(8)
	v_mfma_f32_16x16x32_f16 v[26:29], v[176:179], v[26:29], v[46:49]
	s_waitcnt lgkmcnt(2)
	v_mfma_f32_16x16x32_f16 v[46:49], v[162:165], v[196:199], v[50:53]
	v_mfma_f32_16x16x32_f16 v[50:53], v[168:171], v[196:199], v[54:57]
	v_mfma_f32_16x16x32_f16 v[54:57], v[172:175], v[196:199], v[58:61]
	v_mfma_f32_16x16x32_f16 v[58:61], v[176:179], v[196:199], v[62:65]
	s_waitcnt lgkmcnt(1)
	v_mfma_f32_16x16x32_f16 v[62:65], v[162:165], v[200:203], v[66:69]
	v_mfma_f32_16x16x32_f16 v[66:69], v[168:171], v[200:203], v[70:73]
	v_mfma_f32_16x16x32_f16 v[70:73], v[172:175], v[200:203], v[74:77]
	v_mfma_f32_16x16x32_f16 v[74:77], v[176:179], v[200:203], v[78:81]
	s_waitcnt lgkmcnt(0)
	v_mfma_f32_16x16x32_f16 v[78:81], v[162:165], v[204:207], v[82:85]
	v_mfma_f32_16x16x32_f16 v[82:85], v[168:171], v[204:207], v[86:89]
	v_mfma_f32_16x16x32_f16 v[86:89], v[172:175], v[204:207], v[90:93]
	v_mfma_f32_16x16x32_f16 v[90:93], v[176:179], v[204:207], v[94:97]
	s_setprio 0
	s_nop 1
	v_add_u32_e32 v94, 0x10000, v166
	v_add_u32_e32 v167, 0x14000, v166
	ds_read_b128 v[94:97], v94
	ds_read_b128 v[196:199], v167
	v_add_u32_e32 v167, 0x18000, v166
	v_add_u32_e32 v166, 0x1c000, v166
	ds_read_b128 v[200:203], v167
	ds_read_b128 v[204:207], v166
	s_setprio 1
	s_waitcnt lgkmcnt(3)
	v_mfma_f32_16x16x32_f16 v[98:101], v[162:165], v[94:97], v[98:101]
	v_mfma_f32_16x16x32_f16 v[102:105], v[168:171], v[94:97], v[102:105]
	v_mfma_f32_16x16x32_f16 v[106:109], v[172:175], v[94:97], v[106:109]
	v_mfma_f32_16x16x32_f16 v[94:97], v[176:179], v[94:97], v[110:113]
	s_waitcnt lgkmcnt(2)
	v_mfma_f32_16x16x32_f16 v[110:113], v[162:165], v[196:199], v[114:117]
	v_mfma_f32_16x16x32_f16 v[114:117], v[168:171], v[196:199], v[118:121]
	v_mfma_f32_16x16x32_f16 v[118:121], v[172:175], v[196:199], v[122:125]
	v_mfma_f32_16x16x32_f16 v[122:125], v[176:179], v[196:199], v[126:129]
	s_waitcnt lgkmcnt(1)
	v_mfma_f32_16x16x32_f16 v[126:129], v[162:165], v[200:203], v[130:133]
	v_mfma_f32_16x16x32_f16 v[130:133], v[168:171], v[200:203], v[134:137]
	v_mfma_f32_16x16x32_f16 v[134:137], v[172:175], v[200:203], v[138:141]
	v_mfma_f32_16x16x32_f16 v[138:141], v[176:179], v[200:203], v[142:145]
	s_waitcnt lgkmcnt(0)
	v_mfma_f32_16x16x32_f16 v[2:5], v[162:165], v[204:207], v[2:5]
	v_mfma_f32_16x16x32_f16 v[6:9], v[168:171], v[204:207], v[6:9]
	v_mfma_f32_16x16x32_f16 v[10:13], v[172:175], v[204:207], v[10:13]
	v_mfma_f32_16x16x32_f16 v[14:17], v[176:179], v[204:207], v[14:17]
	s_setprio 0
	v_lshl_add_u32 v174, s3, 10, v191
	ds_read_b128 v[142:145], v174
	ds_read_b128 v[162:165], v174 offset:16384
	ds_read_b128 v[166:169], v174 offset:32768
	ds_read_b128 v[170:173], v174 offset:49152
	s_setprio 1
	s_waitcnt vmcnt(7) lgkmcnt(3)
	v_mfma_f32_16x16x32_f16 v[34:37], v[146:149], v[142:145], v[34:37]
	s_waitcnt vmcnt(6)
	v_mfma_f32_16x16x32_f16 v[38:41], v[150:153], v[142:145], v[38:41]
	s_waitcnt vmcnt(5)
	v_mfma_f32_16x16x32_f16 v[42:45], v[154:157], v[142:145], v[42:45]
	s_waitcnt vmcnt(4)
	v_mfma_f32_16x16x32_f16 v[26:29], v[158:161], v[142:145], v[26:29]
	s_waitcnt lgkmcnt(2)
	v_mfma_f32_16x16x32_f16 v[46:49], v[146:149], v[162:165], v[46:49]
	v_mfma_f32_16x16x32_f16 v[50:53], v[150:153], v[162:165], v[50:53]
	v_mfma_f32_16x16x32_f16 v[54:57], v[154:157], v[162:165], v[54:57]
	v_mfma_f32_16x16x32_f16 v[58:61], v[158:161], v[162:165], v[58:61]
	s_waitcnt lgkmcnt(1)
	v_mfma_f32_16x16x32_f16 v[62:65], v[146:149], v[166:169], v[62:65]
	v_mfma_f32_16x16x32_f16 v[66:69], v[150:153], v[166:169], v[66:69]
	v_mfma_f32_16x16x32_f16 v[70:73], v[154:157], v[166:169], v[70:73]
	v_mfma_f32_16x16x32_f16 v[74:77], v[158:161], v[166:169], v[74:77]
	s_waitcnt lgkmcnt(0)
	v_mfma_f32_16x16x32_f16 v[78:81], v[146:149], v[170:173], v[78:81]
	v_mfma_f32_16x16x32_f16 v[82:85], v[150:153], v[170:173], v[82:85]
	v_mfma_f32_16x16x32_f16 v[86:89], v[154:157], v[170:173], v[86:89]
	v_mfma_f32_16x16x32_f16 v[162:165], v[158:161], v[170:173], v[90:93]
	s_setprio 0
	s_nop 1
	v_add_u32_e32 v90, 0x10000, v174
	v_add_u32_e32 v142, 0x14000, v174
	v_add_u32_e32 v166, 0x18000, v174
	v_add_u32_e32 v170, 0x1c000, v174
	ds_read_b128 v[90:93], v90
	ds_read_b128 v[142:145], v142
	ds_read_b128 v[166:169], v166
	ds_read_b128 v[170:173], v170
	s_setprio 1
	s_waitcnt lgkmcnt(0)
	v_mfma_f32_16x16x32_f16 v[2:5], v[146:149], v[170:173], v[2:5]
	v_mfma_f32_16x16x32_f16 v[6:9], v[150:153], v[170:173], v[6:9]
	v_mfma_f32_16x16x32_f16 v[10:13], v[154:157], v[170:173], v[10:13]
	v_mfma_f32_16x16x32_f16 v[14:17], v[158:161], v[170:173], v[14:17]
	v_mfma_f32_16x16x32_f16 v[174:177], v[146:149], v[90:93], v[98:101]
	v_mfma_f32_16x16x32_f16 v[196:199], v[150:153], v[90:93], v[102:105]
	v_mfma_f32_16x16x32_f16 v[200:203], v[154:157], v[90:93], v[106:109]
	v_mfma_f32_16x16x32_f16 v[204:207], v[158:161], v[90:93], v[94:97]
	v_mfma_f32_16x16x32_f16 v[208:211], v[146:149], v[142:145], v[110:113]
	v_mfma_f32_16x16x32_f16 v[212:215], v[150:153], v[142:145], v[114:117]
	v_mfma_f32_16x16x32_f16 v[216:219], v[154:157], v[142:145], v[118:121]
	v_mfma_f32_16x16x32_f16 v[220:223], v[158:161], v[142:145], v[122:125]
	v_mfma_f32_16x16x32_f16 v[224:227], v[146:149], v[166:169], v[126:129]
	v_mfma_f32_16x16x32_f16 v[228:231], v[150:153], v[166:169], v[130:133]
	v_mfma_f32_16x16x32_f16 v[232:235], v[154:157], v[166:169], v[134:137]
	v_mfma_f32_16x16x32_f16 v[166:169], v[158:161], v[166:169], v[138:141]
	s_setprio 0
	v_lshl_add_u32 v158, s7, 10, v191
	ds_read_b128 v[90:93], v158
	ds_read_b128 v[94:97], v158 offset:16384
	ds_read_b128 v[98:101], v158 offset:32768
	ds_read_b128 v[146:149], v158 offset:49152
	s_setprio 1
	s_waitcnt vmcnt(3) lgkmcnt(3)
	v_mfma_f32_16x16x32_f16 v[150:153], v[18:21], v[90:93], v[34:37]
	s_waitcnt vmcnt(2)
	v_mfma_f32_16x16x32_f16 v[138:141], v[22:25], v[90:93], v[38:41]
	s_waitcnt vmcnt(1)
	v_mfma_f32_16x16x32_f16 v[154:157], v[30:33], v[90:93], v[42:45]
	s_waitcnt vmcnt(0)
	v_mfma_f32_16x16x32_f16 v[142:145], v[192:195], v[90:93], v[26:29]
	s_waitcnt lgkmcnt(2)
	v_mfma_f32_16x16x32_f16 v[134:137], v[18:21], v[94:97], v[46:49]
	v_mfma_f32_16x16x32_f16 v[122:125], v[22:25], v[94:97], v[50:53]
	v_mfma_f32_16x16x32_f16 v[130:133], v[30:33], v[94:97], v[54:57]
	v_mfma_f32_16x16x32_f16 v[126:129], v[192:195], v[94:97], v[58:61]
	s_waitcnt lgkmcnt(1)
	v_mfma_f32_16x16x32_f16 v[118:121], v[18:21], v[98:101], v[62:65]
	v_mfma_f32_16x16x32_f16 v[106:109], v[22:25], v[98:101], v[66:69]
	v_mfma_f32_16x16x32_f16 v[114:117], v[30:33], v[98:101], v[70:73]
	v_mfma_f32_16x16x32_f16 v[110:113], v[192:195], v[98:101], v[74:77]
	s_waitcnt lgkmcnt(0)
	v_mfma_f32_16x16x32_f16 v[102:105], v[18:21], v[146:149], v[78:81]
	v_mfma_f32_16x16x32_f16 v[90:93], v[22:25], v[146:149], v[82:85]
	v_mfma_f32_16x16x32_f16 v[98:101], v[30:33], v[146:149], v[86:89]
	v_mfma_f32_16x16x32_f16 v[94:97], v[192:195], v[146:149], v[162:165]
	s_setprio 0
	v_add_u32_e32 v26, 0x10000, v158
	v_add_u32_e32 v34, 0x14000, v158
	v_add_u32_e32 v38, 0x18000, v158
	ds_read_b128 v[26:29], v26
	ds_read_b128 v[34:37], v34
	v_add_u32_e32 v42, 0x1c000, v158
	ds_read_b128 v[38:41], v38
	ds_read_b128 v[146:149], v42
	s_setprio 1
	s_waitcnt lgkmcnt(3)
	v_mfma_f32_16x16x32_f16 v[86:89], v[18:21], v[26:29], v[174:177]
	v_mfma_f32_16x16x32_f16 v[74:77], v[22:25], v[26:29], v[196:199]
	v_mfma_f32_16x16x32_f16 v[82:85], v[30:33], v[26:29], v[200:203]
	v_mfma_f32_16x16x32_f16 v[78:81], v[192:195], v[26:29], v[204:207]
	s_waitcnt lgkmcnt(2)
	v_mfma_f32_16x16x32_f16 v[70:73], v[18:21], v[34:37], v[208:211]
	v_mfma_f32_16x16x32_f16 v[58:61], v[22:25], v[34:37], v[212:215]
	v_mfma_f32_16x16x32_f16 v[66:69], v[30:33], v[34:37], v[216:219]
	v_mfma_f32_16x16x32_f16 v[62:65], v[192:195], v[34:37], v[220:223]
	s_waitcnt lgkmcnt(1)
	v_mfma_f32_16x16x32_f16 v[54:57], v[18:21], v[38:41], v[224:227]
	v_mfma_f32_16x16x32_f16 v[42:45], v[22:25], v[38:41], v[228:231]
	v_mfma_f32_16x16x32_f16 v[50:53], v[30:33], v[38:41], v[232:235]
	v_mfma_f32_16x16x32_f16 v[46:49], v[192:195], v[38:41], v[166:169]
	s_waitcnt lgkmcnt(0)
	v_mfma_f32_16x16x32_f16 v[26:29], v[18:21], v[146:149], v[2:5]
	v_mfma_f32_16x16x32_f16 v[2:5], v[22:25], v[146:149], v[6:9]
	v_mfma_f32_16x16x32_f16 v[22:25], v[30:33], v[146:149], v[10:13]
	v_mfma_f32_16x16x32_f16 v[6:9], v[192:195], v[146:149], v[14:17]
	s_setprio 0
	s_lshl_b64 s[0:1], s[42:43], 2
	s_add_u32 s0, s18, s0
	s_addc_u32 s1, s19, s1
	s_lshl_b32 s2, s42, 8
	s_ashr_i32 s3, s2, 31
	v_lshlrev_b32_e32 v146, 5, v187
	s_lshl_b64 s[2:3], s[2:3], 2
	v_and_or_b32 v10, v190, 12, v146
	s_add_u32 s12, s12, s2
	s_addc_u32 s13, s13, s3
	v_lshlrev_b32_e32 v10, 2, v10
	v_add_u32_e32 v254, 0x22640, v10
	ds_read_b128 v[34:37], v254
	ds_read_b128 v[14:17], v254 offset:64
	ds_read_b128 v[38:41], v254 offset:1024
	ds_read_b128 v[18:21], v254 offset:1088
	ds_read_b128 v[30:33], v254 offset:2048
	ds_read_b128 v[10:13], v254 offset:2112
	s_add_u32 s12, s14, s2
	s_addc_u32 s13, s15, s3
	s_add_u32 s2, s16, s2
	s_addc_u32 s3, s17, s3
	s_nop 0
	v_cmp_gt_u32_e32 vcc, 16, v189
	s_mov_b32 s2, s69
	v_mov_b32_e32 v216, 0x3d38aa3b
	v_mov_b32_e32 v217, 0x3d38aa3b
	v_mov_b32_e32 v218, 0xbcb8aa3b
	v_mov_b32_e32 v219, 0xbcb8aa3b
	v_mov_b32_e32 v222, 1.0
	v_mov_b32_e32 v223, 1.0
	v_mov_b32_e32 v224, 0x4038aa3b
	v_mov_b32_e32 v225, 0x4038aa3b
	v_mov_b32_e32 v226, 0xbfb8aa3b
	v_mov_b32_e32 v227, 0xbfb8aa3b
	v_lshlrev_b32_e32 v232, 9, v187
	v_lshlrev_b32_e32 v233, 2, v188
	v_add3_u32 v232, s24, v232, v233
	s_waitcnt vmcnt(0) lgkmcnt(0)
	v_pk_mul_f32 v[34:35], v[34:35], v[224:225]
	v_pk_mul_f32 v[36:37], v[36:37], v[224:225]
	v_pk_mul_f32 v[14:15], v[14:15], v[224:225]
	v_pk_mul_f32 v[16:17], v[16:17], v[224:225]
	v_pk_mul_f32 v[38:39], v[38:39], v[226:227]
	v_pk_mul_f32 v[40:41], v[40:41], v[226:227]
	v_pk_mul_f32 v[18:19], v[18:19], v[226:227]
	v_pk_mul_f32 v[20:21], v[20:21], v[226:227]
	v_pk_fma_f32 v[150:151], v[150:151], v[216:217], v[34:35]
	v_pk_fma_f32 v[154:155], v[154:155], v[218:219], v[38:39]
	v_min_f32_e32 v150, 0x42700000, v150
	v_min_f32_e32 v151, 0x42700000, v151
	v_min_f32_e32 v154, 0x42700000, v154
	v_min_f32_e32 v155, 0x42700000, v155
	v_pk_fma_f32 v[152:153], v[152:153], v[216:217], v[36:37]
	v_pk_fma_f32 v[156:157], v[156:157], v[218:219], v[40:41]
	v_min_f32_e32 v152, 0x42700000, v152
	v_min_f32_e32 v153, 0x42700000, v153
	v_min_f32_e32 v156, 0x42700000, v156
	v_min_f32_e32 v157, 0x42700000, v157
	v_exp_f32_e32 v150, v150
	v_exp_f32_e32 v151, v151
	v_exp_f32_e32 v154, v154
	v_exp_f32_e32 v155, v155
	v_exp_f32_e32 v152, v152
	v_exp_f32_e32 v153, v153
	v_exp_f32_e32 v156, v156
	v_exp_f32_e32 v157, v157
	v_pk_fma_f32 v[228:229], v[150:151], v[30:31], v[30:31] neg_lo:[0,0,1] neg_hi:[0,0,1]
	v_pk_add_f32 v[154:155], v[154:155], v[222:223]
	v_pk_fma_f32 v[150:151], v[150:151], v[154:155], v[154:155]
	v_pk_fma_f32 v[230:231], v[152:153], v[32:33], v[32:33] neg_lo:[0,0,1] neg_hi:[0,0,1]
	v_pk_add_f32 v[156:157], v[156:157], v[222:223]
	v_pk_fma_f32 v[152:153], v[152:153], v[156:157], v[156:157]
	v_rcp_f32_e32 v150, v150
	v_rcp_f32_e32 v151, v151
	v_rcp_f32_e32 v152, v152
	v_rcp_f32_e32 v153, v153
	v_pk_mul_f32 v[200:201], v[228:229], v[150:151]
	v_pk_fma_f32 v[200:201], v[230:231], v[152:153], v[200:201]
	v_pk_fma_f32 v[138:139], v[138:139], v[216:217], v[14:15]
	v_pk_fma_f32 v[142:143], v[142:143], v[218:219], v[18:19]
	v_min_f32_e32 v138, 0x42700000, v138
	v_min_f32_e32 v139, 0x42700000, v139
	v_min_f32_e32 v142, 0x42700000, v142
	v_min_f32_e32 v143, 0x42700000, v143
	v_pk_fma_f32 v[140:141], v[140:141], v[216:217], v[16:17]
	v_pk_fma_f32 v[144:145], v[144:145], v[218:219], v[20:21]
	v_min_f32_e32 v140, 0x42700000, v140
	v_min_f32_e32 v141, 0x42700000, v141
	v_min_f32_e32 v144, 0x42700000, v144
	v_min_f32_e32 v145, 0x42700000, v145
	v_exp_f32_e32 v138, v138
	v_exp_f32_e32 v139, v139
	v_exp_f32_e32 v142, v142
	v_exp_f32_e32 v143, v143
	v_exp_f32_e32 v140, v140
	v_exp_f32_e32 v141, v141
	v_exp_f32_e32 v144, v144
	v_exp_f32_e32 v145, v145
	v_pk_fma_f32 v[228:229], v[138:139], v[10:11], v[10:11] neg_lo:[0,0,1] neg_hi:[0,0,1]
	v_pk_add_f32 v[142:143], v[142:143], v[222:223]
	v_pk_fma_f32 v[138:139], v[138:139], v[142:143], v[142:143]
	v_pk_fma_f32 v[230:231], v[140:141], v[12:13], v[12:13] neg_lo:[0,0,1] neg_hi:[0,0,1]
	v_pk_add_f32 v[144:145], v[144:145], v[222:223]
	v_pk_fma_f32 v[140:141], v[140:141], v[144:145], v[144:145]
	v_rcp_f32_e32 v138, v138
	v_rcp_f32_e32 v139, v139
	v_rcp_f32_e32 v140, v140
	v_rcp_f32_e32 v141, v141
	v_pk_fma_f32 v[200:201], v[228:229], v[138:139], v[200:201]
	v_pk_fma_f32 v[200:201], v[230:231], v[140:141], v[200:201]
	v_pk_fma_f32 v[134:135], v[134:135], v[216:217], v[34:35]
	v_pk_fma_f32 v[130:131], v[130:131], v[218:219], v[38:39]
	v_min_f32_e32 v134, 0x42700000, v134
	v_min_f32_e32 v135, 0x42700000, v135
	v_min_f32_e32 v130, 0x42700000, v130
	v_min_f32_e32 v131, 0x42700000, v131
	v_pk_fma_f32 v[136:137], v[136:137], v[216:217], v[36:37]
	v_pk_fma_f32 v[132:133], v[132:133], v[218:219], v[40:41]
	v_min_f32_e32 v136, 0x42700000, v136
	v_min_f32_e32 v137, 0x42700000, v137
	v_min_f32_e32 v132, 0x42700000, v132
	v_min_f32_e32 v133, 0x42700000, v133
	v_exp_f32_e32 v134, v134
	v_exp_f32_e32 v135, v135
	v_exp_f32_e32 v130, v130
	v_exp_f32_e32 v131, v131
	v_exp_f32_e32 v136, v136
	v_exp_f32_e32 v137, v137
	v_exp_f32_e32 v132, v132
	v_exp_f32_e32 v133, v133
	v_pk_fma_f32 v[228:229], v[134:135], v[30:31], v[30:31] neg_lo:[0,0,1] neg_hi:[0,0,1]
	v_pk_add_f32 v[130:131], v[130:131], v[222:223]
	v_pk_fma_f32 v[134:135], v[134:135], v[130:131], v[130:131]
	v_pk_fma_f32 v[230:231], v[136:137], v[32:33], v[32:33] neg_lo:[0,0,1] neg_hi:[0,0,1]
	v_pk_add_f32 v[132:133], v[132:133], v[222:223]
	v_pk_fma_f32 v[136:137], v[136:137], v[132:133], v[132:133]
	v_rcp_f32_e32 v134, v134
	v_rcp_f32_e32 v135, v135
	v_rcp_f32_e32 v136, v136
	v_rcp_f32_e32 v137, v137
	v_pk_mul_f32 v[202:203], v[228:229], v[134:135]
	v_pk_fma_f32 v[202:203], v[230:231], v[136:137], v[202:203]
	v_pk_fma_f32 v[122:123], v[122:123], v[216:217], v[14:15]
	v_pk_fma_f32 v[126:127], v[126:127], v[218:219], v[18:19]
	v_min_f32_e32 v122, 0x42700000, v122
	v_min_f32_e32 v123, 0x42700000, v123
	v_min_f32_e32 v126, 0x42700000, v126
	v_min_f32_e32 v127, 0x42700000, v127
	v_pk_fma_f32 v[124:125], v[124:125], v[216:217], v[16:17]
	v_pk_fma_f32 v[128:129], v[128:129], v[218:219], v[20:21]
	v_min_f32_e32 v124, 0x42700000, v124
	v_min_f32_e32 v125, 0x42700000, v125
	v_min_f32_e32 v128, 0x42700000, v128
	v_min_f32_e32 v129, 0x42700000, v129
	v_exp_f32_e32 v122, v122
	v_exp_f32_e32 v123, v123
	v_exp_f32_e32 v126, v126
	v_exp_f32_e32 v127, v127
	v_exp_f32_e32 v124, v124
	v_exp_f32_e32 v125, v125
	v_exp_f32_e32 v128, v128
	v_exp_f32_e32 v129, v129
	v_pk_fma_f32 v[228:229], v[122:123], v[10:11], v[10:11] neg_lo:[0,0,1] neg_hi:[0,0,1]
	v_pk_add_f32 v[126:127], v[126:127], v[222:223]
	v_pk_fma_f32 v[122:123], v[122:123], v[126:127], v[126:127]
	v_pk_fma_f32 v[230:231], v[124:125], v[12:13], v[12:13] neg_lo:[0,0,1] neg_hi:[0,0,1]
	v_pk_add_f32 v[128:129], v[128:129], v[222:223]
	v_pk_fma_f32 v[124:125], v[124:125], v[128:129], v[128:129]
	v_rcp_f32_e32 v122, v122
	v_rcp_f32_e32 v123, v123
	v_rcp_f32_e32 v124, v124
	v_rcp_f32_e32 v125, v125
	v_pk_fma_f32 v[202:203], v[228:229], v[122:123], v[202:203]
	v_pk_fma_f32 v[202:203], v[230:231], v[124:125], v[202:203]
	v_pk_fma_f32 v[118:119], v[118:119], v[216:217], v[34:35]
	v_pk_fma_f32 v[114:115], v[114:115], v[218:219], v[38:39]
	v_min_f32_e32 v118, 0x42700000, v118
	v_min_f32_e32 v119, 0x42700000, v119
	v_min_f32_e32 v114, 0x42700000, v114
	v_min_f32_e32 v115, 0x42700000, v115
	v_pk_fma_f32 v[120:121], v[120:121], v[216:217], v[36:37]
	v_pk_fma_f32 v[116:117], v[116:117], v[218:219], v[40:41]
	v_min_f32_e32 v120, 0x42700000, v120
	v_min_f32_e32 v121, 0x42700000, v121
	v_min_f32_e32 v116, 0x42700000, v116
	v_min_f32_e32 v117, 0x42700000, v117
	v_exp_f32_e32 v118, v118
	v_exp_f32_e32 v119, v119
	v_exp_f32_e32 v114, v114
	v_exp_f32_e32 v115, v115
	v_exp_f32_e32 v120, v120
	v_exp_f32_e32 v121, v121
	v_exp_f32_e32 v116, v116
	v_exp_f32_e32 v117, v117
	v_pk_fma_f32 v[228:229], v[118:119], v[30:31], v[30:31] neg_lo:[0,0,1] neg_hi:[0,0,1]
	v_pk_add_f32 v[114:115], v[114:115], v[222:223]
	v_pk_fma_f32 v[118:119], v[118:119], v[114:115], v[114:115]
	v_pk_fma_f32 v[230:231], v[120:121], v[32:33], v[32:33] neg_lo:[0,0,1] neg_hi:[0,0,1]
	v_pk_add_f32 v[116:117], v[116:117], v[222:223]
	v_pk_fma_f32 v[120:121], v[120:121], v[116:117], v[116:117]
	v_rcp_f32_e32 v118, v118
	v_rcp_f32_e32 v119, v119
	v_rcp_f32_e32 v120, v120
	v_rcp_f32_e32 v121, v121
	v_pk_mul_f32 v[204:205], v[228:229], v[118:119]
	v_pk_fma_f32 v[204:205], v[230:231], v[120:121], v[204:205]
	v_pk_fma_f32 v[106:107], v[106:107], v[216:217], v[14:15]
	v_pk_fma_f32 v[110:111], v[110:111], v[218:219], v[18:19]
	v_min_f32_e32 v106, 0x42700000, v106
	v_min_f32_e32 v107, 0x42700000, v107
	v_min_f32_e32 v110, 0x42700000, v110
	v_min_f32_e32 v111, 0x42700000, v111
	v_pk_fma_f32 v[108:109], v[108:109], v[216:217], v[16:17]
	v_pk_fma_f32 v[112:113], v[112:113], v[218:219], v[20:21]
	v_min_f32_e32 v108, 0x42700000, v108
	v_min_f32_e32 v109, 0x42700000, v109
	v_min_f32_e32 v112, 0x42700000, v112
	v_min_f32_e32 v113, 0x42700000, v113
	v_exp_f32_e32 v106, v106
	v_exp_f32_e32 v107, v107
	v_exp_f32_e32 v110, v110
	v_exp_f32_e32 v111, v111
	v_exp_f32_e32 v108, v108
	v_exp_f32_e32 v109, v109
	v_exp_f32_e32 v112, v112
	v_exp_f32_e32 v113, v113
	v_pk_fma_f32 v[228:229], v[106:107], v[10:11], v[10:11] neg_lo:[0,0,1] neg_hi:[0,0,1]
	v_pk_add_f32 v[110:111], v[110:111], v[222:223]
	v_pk_fma_f32 v[106:107], v[106:107], v[110:111], v[110:111]
	v_pk_fma_f32 v[230:231], v[108:109], v[12:13], v[12:13] neg_lo:[0,0,1] neg_hi:[0,0,1]
	v_pk_add_f32 v[112:113], v[112:113], v[222:223]
	v_pk_fma_f32 v[108:109], v[108:109], v[112:113], v[112:113]
	v_rcp_f32_e32 v106, v106
	v_rcp_f32_e32 v107, v107
	v_rcp_f32_e32 v108, v108
	v_rcp_f32_e32 v109, v109
	v_pk_fma_f32 v[204:205], v[228:229], v[106:107], v[204:205]
	v_pk_fma_f32 v[204:205], v[230:231], v[108:109], v[204:205]
	v_pk_fma_f32 v[102:103], v[102:103], v[216:217], v[34:35]
	v_pk_fma_f32 v[98:99], v[98:99], v[218:219], v[38:39]
	v_min_f32_e32 v102, 0x42700000, v102
	v_min_f32_e32 v103, 0x42700000, v103
	v_min_f32_e32 v98, 0x42700000, v98
	v_min_f32_e32 v99, 0x42700000, v99
	v_pk_fma_f32 v[104:105], v[104:105], v[216:217], v[36:37]
	v_pk_fma_f32 v[100:101], v[100:101], v[218:219], v[40:41]
	v_min_f32_e32 v104, 0x42700000, v104
	v_min_f32_e32 v105, 0x42700000, v105
	v_min_f32_e32 v100, 0x42700000, v100
	v_min_f32_e32 v101, 0x42700000, v101
	v_exp_f32_e32 v102, v102
	v_exp_f32_e32 v103, v103
	v_exp_f32_e32 v98, v98
	v_exp_f32_e32 v99, v99
	v_exp_f32_e32 v104, v104
	v_exp_f32_e32 v105, v105
	v_exp_f32_e32 v100, v100
	v_exp_f32_e32 v101, v101
	v_pk_fma_f32 v[228:229], v[102:103], v[30:31], v[30:31] neg_lo:[0,0,1] neg_hi:[0,0,1]
	v_pk_add_f32 v[98:99], v[98:99], v[222:223]
	v_pk_fma_f32 v[102:103], v[102:103], v[98:99], v[98:99]
	v_pk_fma_f32 v[230:231], v[104:105], v[32:33], v[32:33] neg_lo:[0,0,1] neg_hi:[0,0,1]
	v_pk_add_f32 v[100:101], v[100:101], v[222:223]
	v_pk_fma_f32 v[104:105], v[104:105], v[100:101], v[100:101]
	v_rcp_f32_e32 v102, v102
	v_rcp_f32_e32 v103, v103
	v_rcp_f32_e32 v104, v104
	v_rcp_f32_e32 v105, v105
	v_pk_mul_f32 v[206:207], v[228:229], v[102:103]
	v_pk_fma_f32 v[206:207], v[230:231], v[104:105], v[206:207]
	v_pk_fma_f32 v[90:91], v[90:91], v[216:217], v[14:15]
	v_pk_fma_f32 v[94:95], v[94:95], v[218:219], v[18:19]
	v_min_f32_e32 v90, 0x42700000, v90
	v_min_f32_e32 v91, 0x42700000, v91
	v_min_f32_e32 v94, 0x42700000, v94
	v_min_f32_e32 v95, 0x42700000, v95
	v_pk_fma_f32 v[92:93], v[92:93], v[216:217], v[16:17]
	v_pk_fma_f32 v[96:97], v[96:97], v[218:219], v[20:21]
	v_min_f32_e32 v92, 0x42700000, v92
	v_min_f32_e32 v93, 0x42700000, v93
	v_min_f32_e32 v96, 0x42700000, v96
	v_min_f32_e32 v97, 0x42700000, v97
	v_exp_f32_e32 v90, v90
	v_exp_f32_e32 v91, v91
	v_exp_f32_e32 v94, v94
	v_exp_f32_e32 v95, v95
	v_exp_f32_e32 v92, v92
	v_exp_f32_e32 v93, v93
	v_exp_f32_e32 v96, v96
	v_exp_f32_e32 v97, v97
	v_pk_fma_f32 v[228:229], v[90:91], v[10:11], v[10:11] neg_lo:[0,0,1] neg_hi:[0,0,1]
	v_pk_add_f32 v[94:95], v[94:95], v[222:223]
	v_pk_fma_f32 v[90:91], v[90:91], v[94:95], v[94:95]
	v_pk_fma_f32 v[230:231], v[92:93], v[12:13], v[12:13] neg_lo:[0,0,1] neg_hi:[0,0,1]
	v_pk_add_f32 v[96:97], v[96:97], v[222:223]
	v_pk_fma_f32 v[92:93], v[92:93], v[96:97], v[96:97]
	v_rcp_f32_e32 v90, v90
	v_rcp_f32_e32 v91, v91
	v_rcp_f32_e32 v92, v92
	v_rcp_f32_e32 v93, v93
	v_pk_fma_f32 v[206:207], v[228:229], v[90:91], v[206:207]
	v_pk_fma_f32 v[206:207], v[230:231], v[92:93], v[206:207]
	v_pk_fma_f32 v[86:87], v[86:87], v[216:217], v[34:35]
	v_pk_fma_f32 v[82:83], v[82:83], v[218:219], v[38:39]
	v_min_f32_e32 v86, 0x42700000, v86
	v_min_f32_e32 v87, 0x42700000, v87
	v_min_f32_e32 v82, 0x42700000, v82
	v_min_f32_e32 v83, 0x42700000, v83
	v_pk_fma_f32 v[88:89], v[88:89], v[216:217], v[36:37]
	v_pk_fma_f32 v[84:85], v[84:85], v[218:219], v[40:41]
	v_min_f32_e32 v88, 0x42700000, v88
	v_min_f32_e32 v89, 0x42700000, v89
	v_min_f32_e32 v84, 0x42700000, v84
	v_min_f32_e32 v85, 0x42700000, v85
	v_exp_f32_e32 v86, v86
	v_exp_f32_e32 v87, v87
	v_exp_f32_e32 v82, v82
	v_exp_f32_e32 v83, v83
	v_exp_f32_e32 v88, v88
	v_exp_f32_e32 v89, v89
	v_exp_f32_e32 v84, v84
	v_exp_f32_e32 v85, v85
	v_pk_fma_f32 v[228:229], v[86:87], v[30:31], v[30:31] neg_lo:[0,0,1] neg_hi:[0,0,1]
	v_pk_add_f32 v[82:83], v[82:83], v[222:223]
	v_pk_fma_f32 v[86:87], v[86:87], v[82:83], v[82:83]
	v_pk_fma_f32 v[230:231], v[88:89], v[32:33], v[32:33] neg_lo:[0,0,1] neg_hi:[0,0,1]
	v_pk_add_f32 v[84:85], v[84:85], v[222:223]
	v_pk_fma_f32 v[88:89], v[88:89], v[84:85], v[84:85]
	v_rcp_f32_e32 v86, v86
	v_rcp_f32_e32 v87, v87
	v_rcp_f32_e32 v88, v88
	v_rcp_f32_e32 v89, v89
	v_pk_mul_f32 v[208:209], v[228:229], v[86:87]
	v_pk_fma_f32 v[208:209], v[230:231], v[88:89], v[208:209]
	v_pk_fma_f32 v[74:75], v[74:75], v[216:217], v[14:15]
	v_pk_fma_f32 v[78:79], v[78:79], v[218:219], v[18:19]
	v_min_f32_e32 v74, 0x42700000, v74
	v_min_f32_e32 v75, 0x42700000, v75
	v_min_f32_e32 v78, 0x42700000, v78
	v_min_f32_e32 v79, 0x42700000, v79
	v_pk_fma_f32 v[76:77], v[76:77], v[216:217], v[16:17]
	v_pk_fma_f32 v[80:81], v[80:81], v[218:219], v[20:21]
	v_min_f32_e32 v76, 0x42700000, v76
	v_min_f32_e32 v77, 0x42700000, v77
	v_min_f32_e32 v80, 0x42700000, v80
	v_min_f32_e32 v81, 0x42700000, v81
	v_exp_f32_e32 v74, v74
	v_exp_f32_e32 v75, v75
	v_exp_f32_e32 v78, v78
	v_exp_f32_e32 v79, v79
	v_exp_f32_e32 v76, v76
	v_exp_f32_e32 v77, v77
	v_exp_f32_e32 v80, v80
	v_exp_f32_e32 v81, v81
	v_pk_fma_f32 v[228:229], v[74:75], v[10:11], v[10:11] neg_lo:[0,0,1] neg_hi:[0,0,1]
	v_pk_add_f32 v[78:79], v[78:79], v[222:223]
	v_pk_fma_f32 v[74:75], v[74:75], v[78:79], v[78:79]
	v_pk_fma_f32 v[230:231], v[76:77], v[12:13], v[12:13] neg_lo:[0,0,1] neg_hi:[0,0,1]
	v_pk_add_f32 v[80:81], v[80:81], v[222:223]
	v_pk_fma_f32 v[76:77], v[76:77], v[80:81], v[80:81]
	v_rcp_f32_e32 v74, v74
	v_rcp_f32_e32 v75, v75
	v_rcp_f32_e32 v76, v76
	v_rcp_f32_e32 v77, v77
	v_pk_fma_f32 v[208:209], v[228:229], v[74:75], v[208:209]
	v_pk_fma_f32 v[208:209], v[230:231], v[76:77], v[208:209]
	v_pk_fma_f32 v[70:71], v[70:71], v[216:217], v[34:35]
	v_pk_fma_f32 v[66:67], v[66:67], v[218:219], v[38:39]
	v_min_f32_e32 v70, 0x42700000, v70
	v_min_f32_e32 v71, 0x42700000, v71
	v_min_f32_e32 v66, 0x42700000, v66
	v_min_f32_e32 v67, 0x42700000, v67
	v_pk_fma_f32 v[72:73], v[72:73], v[216:217], v[36:37]
	v_pk_fma_f32 v[68:69], v[68:69], v[218:219], v[40:41]
	v_min_f32_e32 v72, 0x42700000, v72
	v_min_f32_e32 v73, 0x42700000, v73
	v_min_f32_e32 v68, 0x42700000, v68
	v_min_f32_e32 v69, 0x42700000, v69
	v_exp_f32_e32 v70, v70
	v_exp_f32_e32 v71, v71
	v_exp_f32_e32 v66, v66
	v_exp_f32_e32 v67, v67
	v_exp_f32_e32 v72, v72
	v_exp_f32_e32 v73, v73
	v_exp_f32_e32 v68, v68
	v_exp_f32_e32 v69, v69
	v_pk_fma_f32 v[228:229], v[70:71], v[30:31], v[30:31] neg_lo:[0,0,1] neg_hi:[0,0,1]
	v_pk_add_f32 v[66:67], v[66:67], v[222:223]
	v_pk_fma_f32 v[70:71], v[70:71], v[66:67], v[66:67]
	v_pk_fma_f32 v[230:231], v[72:73], v[32:33], v[32:33] neg_lo:[0,0,1] neg_hi:[0,0,1]
	v_pk_add_f32 v[68:69], v[68:69], v[222:223]
	v_pk_fma_f32 v[72:73], v[72:73], v[68:69], v[68:69]
	v_rcp_f32_e32 v70, v70
	v_rcp_f32_e32 v71, v71
	v_rcp_f32_e32 v72, v72
	v_rcp_f32_e32 v73, v73
	v_pk_mul_f32 v[210:211], v[228:229], v[70:71]
	v_pk_fma_f32 v[210:211], v[230:231], v[72:73], v[210:211]
	v_pk_fma_f32 v[58:59], v[58:59], v[216:217], v[14:15]
	v_pk_fma_f32 v[62:63], v[62:63], v[218:219], v[18:19]
	v_min_f32_e32 v58, 0x42700000, v58
	v_min_f32_e32 v59, 0x42700000, v59
	v_min_f32_e32 v62, 0x42700000, v62
	v_min_f32_e32 v63, 0x42700000, v63
	v_pk_fma_f32 v[60:61], v[60:61], v[216:217], v[16:17]
	v_pk_fma_f32 v[64:65], v[64:65], v[218:219], v[20:21]
	v_min_f32_e32 v60, 0x42700000, v60
	v_min_f32_e32 v61, 0x42700000, v61
	v_min_f32_e32 v64, 0x42700000, v64
	v_min_f32_e32 v65, 0x42700000, v65
	v_exp_f32_e32 v58, v58
	v_exp_f32_e32 v59, v59
	v_exp_f32_e32 v62, v62
	v_exp_f32_e32 v63, v63
	v_exp_f32_e32 v60, v60
	v_exp_f32_e32 v61, v61
	v_exp_f32_e32 v64, v64
	v_exp_f32_e32 v65, v65
	v_pk_fma_f32 v[228:229], v[58:59], v[10:11], v[10:11] neg_lo:[0,0,1] neg_hi:[0,0,1]
	v_pk_add_f32 v[62:63], v[62:63], v[222:223]
	v_pk_fma_f32 v[58:59], v[58:59], v[62:63], v[62:63]
	v_pk_fma_f32 v[230:231], v[60:61], v[12:13], v[12:13] neg_lo:[0,0,1] neg_hi:[0,0,1]
	v_pk_add_f32 v[64:65], v[64:65], v[222:223]
	v_pk_fma_f32 v[60:61], v[60:61], v[64:65], v[64:65]
	v_rcp_f32_e32 v58, v58
	v_rcp_f32_e32 v59, v59
	v_rcp_f32_e32 v60, v60
	v_rcp_f32_e32 v61, v61
	v_pk_fma_f32 v[210:211], v[228:229], v[58:59], v[210:211]
	v_pk_fma_f32 v[210:211], v[230:231], v[60:61], v[210:211]
	v_pk_fma_f32 v[54:55], v[54:55], v[216:217], v[34:35]
	v_pk_fma_f32 v[50:51], v[50:51], v[218:219], v[38:39]
	v_min_f32_e32 v54, 0x42700000, v54
	v_min_f32_e32 v55, 0x42700000, v55
	v_min_f32_e32 v50, 0x42700000, v50
	v_min_f32_e32 v51, 0x42700000, v51
	v_pk_fma_f32 v[56:57], v[56:57], v[216:217], v[36:37]
	v_pk_fma_f32 v[52:53], v[52:53], v[218:219], v[40:41]
	v_min_f32_e32 v56, 0x42700000, v56
	v_min_f32_e32 v57, 0x42700000, v57
	v_min_f32_e32 v52, 0x42700000, v52
	v_min_f32_e32 v53, 0x42700000, v53
	v_exp_f32_e32 v54, v54
	v_exp_f32_e32 v55, v55
	v_exp_f32_e32 v50, v50
	v_exp_f32_e32 v51, v51
	v_exp_f32_e32 v56, v56
	v_exp_f32_e32 v57, v57
	v_exp_f32_e32 v52, v52
	v_exp_f32_e32 v53, v53
	v_pk_fma_f32 v[228:229], v[54:55], v[30:31], v[30:31] neg_lo:[0,0,1] neg_hi:[0,0,1]
	v_pk_add_f32 v[50:51], v[50:51], v[222:223]
	v_pk_fma_f32 v[54:55], v[54:55], v[50:51], v[50:51]
	v_pk_fma_f32 v[230:231], v[56:57], v[32:33], v[32:33] neg_lo:[0,0,1] neg_hi:[0,0,1]
	v_pk_add_f32 v[52:53], v[52:53], v[222:223]
	v_pk_fma_f32 v[56:57], v[56:57], v[52:53], v[52:53]
	v_rcp_f32_e32 v54, v54
	v_rcp_f32_e32 v55, v55
	v_rcp_f32_e32 v56, v56
	v_rcp_f32_e32 v57, v57
	v_pk_mul_f32 v[212:213], v[228:229], v[54:55]
	v_pk_fma_f32 v[212:213], v[230:231], v[56:57], v[212:213]
	v_pk_fma_f32 v[42:43], v[42:43], v[216:217], v[14:15]
	v_pk_fma_f32 v[46:47], v[46:47], v[218:219], v[18:19]
	v_min_f32_e32 v42, 0x42700000, v42
	v_min_f32_e32 v43, 0x42700000, v43
	v_min_f32_e32 v46, 0x42700000, v46
	v_min_f32_e32 v47, 0x42700000, v47
	v_pk_fma_f32 v[44:45], v[44:45], v[216:217], v[16:17]
	v_pk_fma_f32 v[48:49], v[48:49], v[218:219], v[20:21]
	v_min_f32_e32 v44, 0x42700000, v44
	v_min_f32_e32 v45, 0x42700000, v45
	v_min_f32_e32 v48, 0x42700000, v48
	v_min_f32_e32 v49, 0x42700000, v49
	v_exp_f32_e32 v42, v42
	v_exp_f32_e32 v43, v43
	v_exp_f32_e32 v46, v46
	v_exp_f32_e32 v47, v47
	v_exp_f32_e32 v44, v44
	v_exp_f32_e32 v45, v45
	v_exp_f32_e32 v48, v48
	v_exp_f32_e32 v49, v49
	v_pk_fma_f32 v[228:229], v[42:43], v[10:11], v[10:11] neg_lo:[0,0,1] neg_hi:[0,0,1]
	v_pk_add_f32 v[46:47], v[46:47], v[222:223]
	v_pk_fma_f32 v[42:43], v[42:43], v[46:47], v[46:47]
	v_pk_fma_f32 v[230:231], v[44:45], v[12:13], v[12:13] neg_lo:[0,0,1] neg_hi:[0,0,1]
	v_pk_add_f32 v[48:49], v[48:49], v[222:223]
	v_pk_fma_f32 v[44:45], v[44:45], v[48:49], v[48:49]
	v_rcp_f32_e32 v42, v42
	v_rcp_f32_e32 v43, v43
	v_rcp_f32_e32 v44, v44
	v_rcp_f32_e32 v45, v45
	v_pk_fma_f32 v[212:213], v[228:229], v[42:43], v[212:213]
	v_pk_fma_f32 v[212:213], v[230:231], v[44:45], v[212:213]
	v_pk_fma_f32 v[26:27], v[26:27], v[216:217], v[34:35]
	v_pk_fma_f32 v[22:23], v[22:23], v[218:219], v[38:39]
	v_min_f32_e32 v26, 0x42700000, v26
	v_min_f32_e32 v27, 0x42700000, v27
	v_min_f32_e32 v22, 0x42700000, v22
	v_min_f32_e32 v23, 0x42700000, v23
	v_pk_fma_f32 v[28:29], v[28:29], v[216:217], v[36:37]
	v_pk_fma_f32 v[24:25], v[24:25], v[218:219], v[40:41]
	v_min_f32_e32 v28, 0x42700000, v28
	v_min_f32_e32 v29, 0x42700000, v29
	v_min_f32_e32 v24, 0x42700000, v24
	v_min_f32_e32 v25, 0x42700000, v25
	v_exp_f32_e32 v26, v26
	v_exp_f32_e32 v27, v27
	v_exp_f32_e32 v22, v22
	v_exp_f32_e32 v23, v23
	v_exp_f32_e32 v28, v28
	v_exp_f32_e32 v29, v29
	v_exp_f32_e32 v24, v24
	v_exp_f32_e32 v25, v25
	v_pk_fma_f32 v[228:229], v[26:27], v[30:31], v[30:31] neg_lo:[0,0,1] neg_hi:[0,0,1]
	v_pk_add_f32 v[22:23], v[22:23], v[222:223]
	v_pk_fma_f32 v[26:27], v[26:27], v[22:23], v[22:23]
	v_pk_fma_f32 v[230:231], v[28:29], v[32:33], v[32:33] neg_lo:[0,0,1] neg_hi:[0,0,1]
	v_pk_add_f32 v[24:25], v[24:25], v[222:223]
	v_pk_fma_f32 v[28:29], v[28:29], v[24:25], v[24:25]
	v_rcp_f32_e32 v26, v26
	v_rcp_f32_e32 v27, v27
	v_rcp_f32_e32 v28, v28
	v_rcp_f32_e32 v29, v29
	v_pk_mul_f32 v[214:215], v[228:229], v[26:27]
	v_pk_fma_f32 v[214:215], v[230:231], v[28:29], v[214:215]
	v_pk_fma_f32 v[2:3], v[2:3], v[216:217], v[14:15]
	v_pk_fma_f32 v[6:7], v[6:7], v[218:219], v[18:19]
	v_min_f32_e32 v2, 0x42700000, v2
	v_min_f32_e32 v3, 0x42700000, v3
	v_min_f32_e32 v6, 0x42700000, v6
	v_min_f32_e32 v7, 0x42700000, v7
	v_pk_fma_f32 v[4:5], v[4:5], v[216:217], v[16:17]
	v_pk_fma_f32 v[8:9], v[8:9], v[218:219], v[20:21]
	v_min_f32_e32 v4, 0x42700000, v4
	v_min_f32_e32 v5, 0x42700000, v5
	v_min_f32_e32 v8, 0x42700000, v8
	v_min_f32_e32 v9, 0x42700000, v9
	v_exp_f32_e32 v2, v2
	v_exp_f32_e32 v3, v3
	v_exp_f32_e32 v6, v6
	v_exp_f32_e32 v7, v7
	v_exp_f32_e32 v4, v4
	v_exp_f32_e32 v5, v5
	v_exp_f32_e32 v8, v8
	v_exp_f32_e32 v9, v9
	v_pk_fma_f32 v[228:229], v[2:3], v[10:11], v[10:11] neg_lo:[0,0,1] neg_hi:[0,0,1]
	v_pk_add_f32 v[6:7], v[6:7], v[222:223]
	v_pk_fma_f32 v[2:3], v[2:3], v[6:7], v[6:7]
	v_pk_fma_f32 v[230:231], v[4:5], v[12:13], v[12:13] neg_lo:[0,0,1] neg_hi:[0,0,1]
	v_pk_add_f32 v[8:9], v[8:9], v[222:223]
	v_pk_fma_f32 v[4:5], v[4:5], v[8:9], v[8:9]
	v_rcp_f32_e32 v2, v2
	v_rcp_f32_e32 v3, v3
	v_rcp_f32_e32 v4, v4
	v_rcp_f32_e32 v5, v5
	v_pk_fma_f32 v[214:215], v[228:229], v[2:3], v[214:215]
	v_pk_fma_f32 v[214:215], v[230:231], v[4:5], v[214:215]
	v_add_f32_e32 v240, v200, v201
	v_add_f32_e32 v241, v202, v203
	v_add_f32_e32 v242, v204, v205
	v_add_f32_e32 v243, v206, v207
	v_add_f32_e32 v244, v208, v209
	v_add_f32_e32 v245, v210, v211
	v_add_f32_e32 v246, v212, v213
	v_add_f32_e32 v247, v214, v215
	ds_bpermute_b32 v200, v181, v240
	ds_bpermute_b32 v201, v181, v241
	ds_bpermute_b32 v202, v181, v242
	ds_bpermute_b32 v203, v181, v243
	ds_bpermute_b32 v204, v181, v244
	ds_bpermute_b32 v205, v181, v245
	ds_bpermute_b32 v206, v181, v246
	ds_bpermute_b32 v207, v181, v247
	s_waitcnt lgkmcnt(0)
	v_add_f32_e32 v240, v240, v200
	v_add_f32_e32 v241, v241, v201
	v_add_f32_e32 v242, v242, v202
	v_add_f32_e32 v243, v243, v203
	v_add_f32_e32 v244, v244, v204
	v_add_f32_e32 v245, v245, v205
	v_add_f32_e32 v246, v246, v206
	v_add_f32_e32 v247, v247, v207
	ds_bpermute_b32 v200, v183, v240
	ds_bpermute_b32 v201, v183, v241
	ds_bpermute_b32 v202, v183, v242
	ds_bpermute_b32 v203, v183, v243
	ds_bpermute_b32 v204, v183, v244
	ds_bpermute_b32 v205, v183, v245
	ds_bpermute_b32 v206, v183, v246
	ds_bpermute_b32 v207, v183, v247
	s_waitcnt lgkmcnt(0)
	v_add_f32_e32 v240, v240, v200
	v_add_f32_e32 v241, v241, v201
	v_add_f32_e32 v242, v242, v202
	v_add_f32_e32 v243, v243, v203
	v_add_f32_e32 v244, v244, v204
	v_add_f32_e32 v245, v245, v205
	v_add_f32_e32 v246, v246, v206
	v_add_f32_e32 v247, v247, v207
	s_and_saveexec_b64 s[64:65], vcc
	ds_write2_b32 v232, v240, v241 offset0:0 offset1:16
	ds_write2_b32 v232, v242, v243 offset0:32 offset1:48
	ds_write2_b32 v232, v244, v245 offset0:64 offset1:80
	ds_write2_b32 v232, v246, v247 offset0:96 offset1:112
	s_mov_b64 exec, s[64:65]
	v_mov_b32_e32 v4, 0
	v_lshlrev_b32_e32 v10, 2, v189
	v_mov_b32_e32 v11, v4
	v_and_b32_e32 v70, 0x1c0, v0
	s_waitcnt lgkmcnt(0)
	v_lshl_add_u64 v[2:3], s[44:45], 0, v[10:11]
	s_lshl_b64 s[0:1], s[42:43], 17
	v_lshlrev_b32_e32 v6, 8, v70
	v_mov_b32_e32 v7, v4
	v_lshl_add_u64 v[2:3], v[2:3], 0, s[0:1]
	v_lshl_add_u64 v[2:3], v[2:3], 0, v[6:7]
	s_movk_i32 s0, 0x1000
	v_add_co_u32_e32 v6, vcc, s0, v2
	s_movk_i32 s0, 0x2000
	s_nop 0
	v_addc_co_u32_e32 v7, vcc, 0, v3, vcc
	v_add_co_u32_e32 v8, vcc, s0, v2
	s_movk_i32 s0, 0x3000
	s_nop 0
	v_addc_co_u32_e32 v9, vcc, 0, v3, vcc
	global_load_dword v78, v[2:3], off
	global_load_dword v77, v[2:3], off offset:256
	global_load_dword v76, v[2:3], off offset:512
	global_load_dword v75, v[2:3], off offset:768
	global_load_dword v74, v[2:3], off offset:1024
	global_load_dword v73, v[2:3], off offset:1280
	global_load_dword v72, v[2:3], off offset:1536
	global_load_dword v71, v[2:3], off offset:1792
	global_load_dword v69, v[2:3], off offset:2048
	global_load_dword v65, v[2:3], off offset:2304
	global_load_dword v63, v[2:3], off offset:2560
	global_load_dword v62, v[2:3], off offset:2816
	global_load_dword v61, v[2:3], off offset:3072
	global_load_dword v51, v[2:3], off offset:3328
	global_load_dword v52, v[2:3], off offset:3584
	global_load_dword v53, v[2:3], off offset:3840
	v_add_co_u32_e32 v2, vcc, s0, v2
	global_load_dword v55, v[6:7], off offset:256
	global_load_dword v56, v[6:7], off offset:512
	global_load_dword v57, v[6:7], off offset:768
	global_load_dword v54, v[6:7], off offset:1024
	global_load_dword v48, v[6:7], off offset:1280
	global_load_dword v49, v[6:7], off offset:1536
	global_load_dword v50, v[6:7], off offset:1792
	global_load_dword v47, v[6:7], off offset:2048
	global_load_dword v43, v[8:9], off
	global_load_dword v44, v[8:9], off offset:256
	global_load_dword v45, v[8:9], off offset:512
	global_load_dword v46, v[8:9], off offset:768
	global_load_dword v42, v[8:9], off offset:1024
	global_load_dword v39, v[8:9], off offset:1280
	global_load_dword v40, v[8:9], off offset:1536
	global_load_dword v41, v[8:9], off offset:1792
	global_load_dword v33, v[8:9], off offset:2048
	global_load_dword v34, v[8:9], off offset:2304
	global_load_dword v35, v[8:9], off offset:2560
	global_load_dword v36, v[8:9], off offset:2816
	global_load_dword v32, v[8:9], off offset:3072
	global_load_dword v24, v[8:9], off offset:3328
	global_load_dword v25, v[8:9], off offset:3584
	global_load_dword v26, v[8:9], off offset:3840
	v_addc_co_u32_e32 v3, vcc, 0, v3, vcc
	global_load_dword v66, v[6:7], off offset:2304
	global_load_dword v67, v[6:7], off offset:2560
	global_load_dword v68, v[6:7], off offset:2816
	global_load_dword v64, v[6:7], off offset:3072
	global_load_dword v58, v[6:7], off offset:3328
	global_load_dword v59, v[6:7], off offset:3584
	global_load_dword v60, v[6:7], off offset:3840
	global_load_dword v28, v[2:3], off
	global_load_dword v29, v[2:3], off offset:256
	global_load_dword v30, v[2:3], off offset:512
	global_load_dword v31, v[2:3], off offset:768
	global_load_dword v27, v[2:3], off offset:1024
	global_load_dword v21, v[2:3], off offset:1280
	global_load_dword v22, v[2:3], off offset:1536
	global_load_dword v23, v[2:3], off offset:1792
	global_load_dword v16, v[2:3], off offset:2048
	global_load_dword v79, v[8:9], off offset:-4096
	global_load_dword v18, v[2:3], off offset:2304
	global_load_dword v19, v[2:3], off offset:2560
	global_load_dword v20, v[2:3], off offset:2816
	global_load_dword v17, v[2:3], off offset:3072
	global_load_dword v15, v[2:3], off offset:3328
	global_load_dword v13, v[2:3], off offset:3584
	global_load_dword v11, v[2:3], off offset:3840
	v_lshl_add_u32 v2, v189, 2, 0
	v_add_u32_e32 v5, 0x20000, v2
	s_waitcnt vmcnt(63) expcnt(7) lgkmcnt(15)
	s_barrier
	ds_read2st64_b32 v[2:3], v5 offset1:1
	ds_read2st64_b32 v[6:7], v5 offset0:2 offset1:3
	ds_read2st64_b32 v[8:9], v5 offset0:4 offset1:5
	ds_read2st64_b32 v[80:81], v5 offset0:6 offset1:7
	s_mov_b32 s7, 0
	s_waitcnt lgkmcnt(3)
	v_add_f32_e32 v2, s2, v2
	v_add_f32_e32 v3, s2, v3
	s_waitcnt lgkmcnt(2)
	v_add_f32_e32 v2, v2, v6
	v_add_f32_e32 v3, v3, v7
	s_waitcnt lgkmcnt(1)
	v_add_f32_e32 v2, v2, v8
	v_add_f32_e32 v6, v3, v9
	s_waitcnt lgkmcnt(0)
	v_add_f32_e32 v12, v2, v80
	ds_read2st64_b32 v[2:3], v5 offset0:8 offset1:9
	v_add_f32_e32 v14, v6, v81
	ds_read2st64_b32 v[6:7], v5 offset0:10 offset1:11
	ds_read2st64_b32 v[8:9], v5 offset0:12 offset1:13
	ds_read2st64_b32 v[80:81], v5 offset0:14 offset1:15
	v_cmp_gt_u32_e64 s[0:1], 64, v0
	s_waitcnt lgkmcnt(3)
	v_add_f32_e32 v2, v12, v2
	v_add_f32_e32 v3, v14, v3
	s_waitcnt lgkmcnt(2)
	v_add_f32_e32 v2, v2, v6
	v_add_f32_e32 v3, v3, v7
	s_waitcnt lgkmcnt(1)
	v_add_f32_e32 v2, v2, v8
	v_add_f32_e32 v3, v3, v9
	s_waitcnt lgkmcnt(0)
	v_add_f32_e32 v2, v2, v80
	v_add_f32_e32 v3, v3, v81
	v_max_f32_e32 v5, v2, v3
	ds_bpermute_b32 v6, v183, v5
	s_waitcnt lgkmcnt(0)
	v_max_f32_e32 v6, v6, v6
	v_max_f32_e32 v5, v5, v6
	ds_bpermute_b32 v6, v181, v5
	s_waitcnt lgkmcnt(0)
	v_max_f32_e32 v6, v6, v6
	v_max_f32_e32 v5, v5, v6
	ds_bpermute_b32 v6, v1, v5
	s_waitcnt lgkmcnt(0)
	v_max_f32_e32 v6, v6, v6
	v_max_f32_e32 v5, v5, v6
	ds_bpermute_b32 v6, v180, v5
	s_waitcnt lgkmcnt(0)
	v_max_f32_e32 v6, v6, v6
	v_max_f32_e32 v5, v5, v6
	ds_bpermute_b32 v6, v182, v5
	s_waitcnt lgkmcnt(0)
	v_max_f32_e32 v6, v6, v6
	v_max_f32_e32 v5, v5, v6
	ds_bpermute_b32 v6, v184, v5
	s_waitcnt lgkmcnt(0)
	v_max_f32_e32 v6, v6, v6
	v_max_f32_e32 v14, v5, v6
	v_sub_f32_e32 v2, v2, v14
	v_sub_f32_e32 v3, v3, v14
	v_mul_f32_e32 v2, 0x3fb8aa3b, v2
	v_mul_f32_e32 v3, 0x3fb8aa3b, v3
	v_exp_f32_e32 v2, v2
	v_exp_f32_e32 v3, v3
	s_nop 0
	v_add_f32_e32 v5, v2, v3
	ds_bpermute_b32 v6, v183, v5
	s_waitcnt lgkmcnt(0)
	v_add_f32_e32 v5, v5, v6
	ds_bpermute_b32 v6, v181, v5
	s_waitcnt lgkmcnt(0)
	v_add_f32_e32 v5, v5, v6
	ds_bpermute_b32 v6, v1, v5
	s_waitcnt lgkmcnt(0)
	v_add_f32_e32 v5, v5, v6
	ds_bpermute_b32 v6, v180, v5
	s_waitcnt lgkmcnt(0)
	v_add_f32_e32 v5, v5, v6
	ds_bpermute_b32 v6, v182, v5
	s_waitcnt lgkmcnt(0)
	v_add_f32_e32 v37, v5, v6
	ds_bpermute_b32 v38, v184, v37
	s_and_saveexec_b64 s[2:3], s[0:1]
	s_cbranch_execz .LBB5_166
	s_add_i32 s12, 0, 0x21000
	v_lshl_add_u32 v5, v189, 2, s12
	v_lshl_add_u32 v6, v0, 2, s12
	ds_write_b32 v5, v2
	ds_write_b32 v6, v3 offset:256

	.amdhsa_kernel _Z8k_expertPKDF16_S0_PKfPcPiS0_S2_S2_S2_S2_PfS5_S4_S2_S2_S2_S2_S5_S2_S2_S2_
		.amdhsa_group_segment_fixed_size 0
		.amdhsa_private_segment_fixed_size 0
		.amdhsa_kernarg_size 168
		.amdhsa_user_sgpr_count 2
		.amdhsa_user_sgpr_dispatch_ptr 0
		.amdhsa_user_sgpr_queue_ptr 0
		.amdhsa_user_sgpr_kernarg_segment_ptr 1
		.amdhsa_user_sgpr_dispatch_id 0
		.amdhsa_user_sgpr_kernarg_preload_length 0
		.amdhsa_user_sgpr_kernarg_preload_offset 0
		.amdhsa_user_sgpr_private_segment_size 0
		.amdhsa_uses_dynamic_stack 0
		.amdhsa_enable_private_segment 0
		.amdhsa_system_sgpr_workgroup_id_x 1
		.amdhsa_system_sgpr_workgroup_id_y 0
		.amdhsa_system_sgpr_workgroup_id_z 0
		.amdhsa_system_sgpr_workgroup_info 0
		.amdhsa_system_vgpr_workitem_id 0
		.amdhsa_next_free_vgpr 256
		.amdhsa_next_free_sgpr 70
		.amdhsa_accum_offset 256
		.amdhsa_reserve_vcc 1
		.amdhsa_float_round_mode_32 0
		.amdhsa_float_round_mode_16_64 0
		.amdhsa_float_denorm_mode_32 3
		.amdhsa_float_denorm_mode_16_64 3
		.amdhsa_dx10_clamp 1
		.amdhsa_ieee_mode 1
		.amdhsa_fp16_overflow 0
		.amdhsa_tg_split 0
		.amdhsa_exception_fp_ieee_invalid_op 0
		.amdhsa_exception_fp_denorm_src 0
		.amdhsa_exception_fp_ieee_div_zero 0
		.amdhsa_exception_fp_ieee_overflow 0
		.amdhsa_exception_fp_ieee_underflow 0
		.amdhsa_exception_fp_ieee_inexact 0
		.amdhsa_exception_int_div_zero 0
	.end_amdhsa_kernel

amdhsa.kernels:
  - .agpr_count:     0
    .args:
      - .actual_access:  read_only
        .address_space:  global
        .offset:         0
        .size:           8
        .value_kind:     global_buffer
      - .actual_access:  read_only
        .address_space:  global
        .offset:         8
        .size:           8
        .value_kind:     global_buffer
      - .actual_access:  read_only
        .address_space:  global
        .offset:         16
        .size:           8
        .value_kind:     global_buffer
      - .actual_access:  write_only
        .address_space:  global
        .offset:         24
        .size:           8
        .value_kind:     global_buffer
      - .actual_access:  write_only
        .address_space:  global
        .offset:         32
        .size:           8
        .value_kind:     global_buffer
      - .actual_access:  read_only
        .address_space:  global
        .offset:         40
        .size:           8
        .value_kind:     global_buffer
      - .actual_access:  read_only
        .address_space:  global
        .offset:         48
        .size:           8
        .value_kind:     global_buffer
      - .actual_access:  read_only
        .address_space:  global
        .offset:         56
        .size:           8
        .value_kind:     global_buffer
      - .actual_access:  read_only
        .address_space:  global
        .offset:         64
        .size:           8
        .value_kind:     global_buffer
      - .actual_access:  read_only
        .address_space:  global
        .offset:         72
        .size:           8
        .value_kind:     global_buffer
      - .actual_access:  read_only
        .address_space:  global
        .offset:         80
        .size:           8
        .value_kind:     global_buffer
    .group_segment_fixed_size: 16384
    .kernarg_segment_align: 8
    .kernarg_segment_size: 88
    .language:       OpenCL C
    .language_version:
      - 2
      - 0
    .max_flat_workgroup_size: 768
    .name:           _Z9k_router2PKfPKDF16_S0_PDF16_PfPiS0_S0_S4_S5_S4_
    .private_segment_fixed_size: 0
    .sgpr_count:     21
    .sgpr_spill_count: 0
    .symbol:         _Z9k_router2PKfPKDF16_S0_PDF16_PfPiS0_S0_S4_S5_S4_.kd
    .uniform_work_group_size: 1
    .uses_dynamic_stack: false
    .vgpr_count:     168
    .vgpr_spill_count: 0
    .wavefront_size: 64
  - .agpr_count:     0
    .args:
      - .actual_access:  read_only
        .address_space:  global
        .offset:         0
        .size:           8
        .value_kind:     global_buffer
      - .actual_access:  read_only
        .address_space:  global
        .offset:         8
        .size:           8
        .value_kind:     global_buffer
      - .actual_access:  read_only
        .address_space:  global
        .offset:         16
        .size:           8
        .value_kind:     global_buffer
      - .actual_access:  write_only
        .address_space:  global
        .offset:         24
        .size:           8
        .value_kind:     global_buffer
      - .actual_access:  write_only
        .address_space:  global
        .offset:         32
        .size:           8
        .value_kind:     global_buffer
      - .actual_access:  write_only
        .address_space:  global
        .offset:         40
        .size:           8
        .value_kind:     global_buffer
    .group_segment_fixed_size: 256
    .kernarg_segment_align: 8
    .kernarg_segment_size: 48
    .language:       OpenCL C
    .language_version:
      - 2
      - 0
    .max_flat_workgroup_size: 256
    .name:           _Z6k_gatePKfS0_S0_PfPiS1_
    .private_segment_fixed_size: 0
    .sgpr_count:     26
    .sgpr_spill_count: 0
    .symbol:         _Z6k_gatePKfS0_S0_PfPiS1_.kd
    .uniform_work_group_size: 1
    .uses_dynamic_stack: false
    .vgpr_count:     51
    .vgpr_spill_count: 0
    .wavefront_size: 64
  - .agpr_count:     0
    .args:
      - .actual_access:  read_only
        .address_space:  global
        .offset:         0
        .size:           8
        .value_kind:     global_buffer
      - .actual_access:  write_only
        .address_space:  global
        .offset:         8
        .size:           8
        .value_kind:     global_buffer
      - .actual_access:  read_only
        .address_space:  global
        .offset:         16
        .size:           8
        .value_kind:     global_buffer
      - .actual_access:  read_only
        .address_space:  global
        .offset:         24
        .size:           8
        .value_kind:     global_buffer
      - .actual_access:  read_only
        .address_space:  global
        .offset:         32
        .size:           8
        .value_kind:     global_buffer
      - .actual_access:  write_only
        .address_space:  global
        .offset:         40
        .size:           8
        .value_kind:     global_buffer
      - .actual_access:  write_only
        .address_space:  global
        .offset:         48
        .size:           8
        .value_kind:     global_buffer
      - .actual_access:  write_only
        .address_space:  global
        .offset:         56
        .size:           8
        .value_kind:     global_buffer
      - .actual_access:  write_only
        .address_space:  global
        .offset:         64
        .size:           8
        .value_kind:     global_buffer
      - .actual_access:  write_only
        .address_space:  global
        .offset:         72
        .size:           8
        .value_kind:     global_buffer
    .group_segment_fixed_size: 16640
    .kernarg_segment_align: 8
    .kernarg_segment_size: 80
    .language:       OpenCL C
    .language_version:
      - 2
      - 0
    .max_flat_workgroup_size: 256
    .name:           _Z10k_prep_allPKfPDF16_S0_S0_S0_S1_S1_PiS2_S2_
    .private_segment_fixed_size: 0
    .sgpr_count:     20
    .sgpr_spill_count: 0
    .symbol:         _Z10k_prep_allPKfPDF16_S0_S0_S0_S1_S1_PiS2_S2_.kd
    .uniform_work_group_size: 1
    .uses_dynamic_stack: false
    .vgpr_count:     37
    .vgpr_spill_count: 0
    .wavefront_size: 64
  - .agpr_count:     0
    .args:
      - .address_space:  global
        .offset:         0
        .size:           8
        .value_kind:     global_buffer
      - .address_space:  global
        .offset:         8
        .size:           8
        .value_kind:     global_buffer
      - .actual_access:  read_only
        .address_space:  global
        .offset:         16
        .size:           8
        .value_kind:     global_buffer
      - .actual_access:  read_only
        .address_space:  global
        .offset:         24
        .size:           8
        .value_kind:     global_buffer
      - .actual_access:  write_only
        .address_space:  global
        .offset:         32
        .size:           8
        .value_kind:     global_buffer
    .group_segment_fixed_size: 0
    .kernarg_segment_align: 8
    .kernarg_segment_size: 40
    .language:       OpenCL C
    .language_version:
      - 2
      - 0
    .max_flat_workgroup_size: 512
    .name:           _Z7k_gemm1PKDF16_S0_PKfPKiPDF16_
    .private_segment_fixed_size: 0
    .sgpr_count:     36
    .sgpr_spill_count: 0
    .symbol:         _Z7k_gemm1PKDF16_S0_PKfPKiPDF16_.kd
    .uniform_work_group_size: 1
    .uses_dynamic_stack: false
    .vgpr_count:     240
    .vgpr_spill_count: 0
    .wavefront_size: 64
  - .agpr_count:     0
    .args:
      - .address_space:  global
        .offset:         0
        .size:           8
        .value_kind:     global_buffer
      - .actual_access:  read_only
        .address_space:  global
        .offset:         8
        .size:           8
        .value_kind:     global_buffer
      - .actual_access:  read_only
        .address_space:  global
        .offset:         16
        .size:           8
        .value_kind:     global_buffer
      - .actual_access:  read_only
        .address_space:  global
        .offset:         24
        .size:           8
        .value_kind:     global_buffer
      - .actual_access:  read_only
        .address_space:  global
        .offset:         32
        .size:           8
        .value_kind:     global_buffer
      - .actual_access:  read_only
        .address_space:  global
        .offset:         40
        .size:           8
        .value_kind:     global_buffer
      - .actual_access:  read_only
        .address_space:  global
        .offset:         48
        .size:           8
        .value_kind:     global_buffer
      - .actual_access:  write_only
        .address_space:  global
        .offset:         56
        .size:           8
        .value_kind:     global_buffer
      - .actual_access:  write_only
        .address_space:  global
        .offset:         64
        .size:           8
        .value_kind:     global_buffer
    .group_segment_fixed_size: 0
    .kernarg_segment_align: 8
    .kernarg_segment_size: 72
    .language:       OpenCL C
    .language_version:
      - 2
      - 0
    .max_flat_workgroup_size: 512
    .name:           _Z11k_gemm2poolPKDF16_S0_PKfS2_S2_S2_PKiPfS5_
    .private_segment_fixed_size: 0
    .sgpr_count:     32
    .sgpr_spill_count: 0
    .symbol:         _Z11k_gemm2poolPKDF16_S0_PKfS2_S2_S2_PKiPfS5_.kd
    .uniform_work_group_size: 1
    .uses_dynamic_stack: false
    .vgpr_count:     198
    .vgpr_spill_count: 0
    .wavefront_size: 64
  - .agpr_count:     0
    .args:
      - .address_space:  global
        .offset:         0
        .size:           8
        .value_kind:     global_buffer
      - .address_space:  global
        .offset:         8
        .size:           8
        .value_kind:     global_buffer
      - .actual_access:  read_only
        .address_space:  global
        .offset:         16
        .size:           8
        .value_kind:     global_buffer
      - .address_space:  global
        .offset:         24
        .size:           8
        .value_kind:     global_buffer
      - .address_space:  global
        .offset:         32
        .size:           8
        .value_kind:     global_buffer
      - .actual_access:  read_only
        .address_space:  global
        .offset:         40
        .size:           8
        .value_kind:     global_buffer
      - .actual_access:  read_only
        .address_space:  global
        .offset:         48
        .size:           8
        .value_kind:     global_buffer
      - .actual_access:  read_only
        .address_space:  global
        .offset:         56
        .size:           8
        .value_kind:     global_buffer
      - .actual_access:  read_only
        .address_space:  global
        .offset:         64
        .size:           8
        .value_kind:     global_buffer
      - .actual_access:  read_only
        .address_space:  global
        .offset:         72
        .size:           8
        .value_kind:     global_buffer
      - .address_space:  global
        .offset:         80
        .size:           8
        .value_kind:     global_buffer
      - .address_space:  global
        .offset:         88
        .size:           8
        .value_kind:     global_buffer
      - .address_space:  global
        .offset:         96
        .size:           8
        .value_kind:     global_buffer
      - .actual_access:  read_only
        .address_space:  global
        .offset:         104
        .size:           8
        .value_kind:     global_buffer
      - .actual_access:  read_only
        .address_space:  global
        .offset:         112
        .size:           8
        .value_kind:     global_buffer
      - .actual_access:  read_only
        .address_space:  global
        .offset:         120
        .size:           8
        .value_kind:     global_buffer
      - .actual_access:  read_only
        .address_space:  global
        .offset:         128
        .size:           8
        .value_kind:     global_buffer
      - .actual_access:  write_only
        .address_space:  global
        .offset:         136
        .size:           8
        .value_kind:     global_buffer
      - .actual_access:  read_only
        .address_space:  global
        .offset:         144
        .size:           8
        .value_kind:     global_buffer
      - .actual_access:  read_only
        .address_space:  global
        .offset:         152
        .size:           8
        .value_kind:     global_buffer
      - .actual_access:  read_only
        .address_space:  global
        .offset:         160
        .size:           8
        .value_kind:     global_buffer
    .group_segment_fixed_size: 0
    .kernarg_segment_align: 8
    .kernarg_segment_size: 168
    .language:       OpenCL C
    .language_version:
      - 2
      - 0
    .max_flat_workgroup_size: 512
    .name:           _Z8k_expertPKDF16_S0_PKfPcPiS0_S2_S2_S2_S2_PfS5_S4_S2_S2_S2_S2_S5_S2_S2_S2_
    .private_segment_fixed_size: 0
    .sgpr_count:     76
    .sgpr_spill_count: 0
    .symbol:         _Z8k_expertPKDF16_S0_PKfPcPiS0_S2_S2_S2_S2_PfS5_S4_S2_S2_S2_S2_S5_S2_S2_S2_.kd
    .uniform_work_group_size: 1
    .uses_dynamic_stack: false
    .vgpr_count:     256
    .vgpr_spill_count: 0
    .wavefront_size: 64
  - .agpr_count:     0
    .args:
      - .actual_access:  read_only
        .address_space:  global
        .offset:         0
        .size:           8
        .value_kind:     global_buffer
      - .actual_access:  read_only
        .address_space:  global
        .offset:         8
        .size:           8
        .value_kind:     global_buffer
      - .actual_access:  read_only
        .address_space:  global
        .offset:         16
        .size:           8
        .value_kind:     global_buffer
      - .actual_access:  read_only
        .address_space:  global
        .offset:         24
        .size:           8
        .value_kind:     global_buffer
      - .actual_access:  read_only
        .address_space:  global
        .offset:         32
        .size:           8
        .value_kind:     global_buffer
      - .actual_access:  read_only
        .address_space:  global
        .offset:         40
        .size:           8
        .value_kind:     global_buffer
      - .actual_access:  read_only
        .address_space:  global
        .offset:         48
        .size:           8
        .value_kind:     global_buffer
      - .actual_access:  read_only
        .address_space:  global
        .offset:         56
        .size:           8
        .value_kind:     global_buffer
      - .actual_access:  write_only
        .address_space:  global
        .offset:         64
        .size:           8
        .value_kind:     global_buffer
    .group_segment_fixed_size: 8768
    .kernarg_segment_align: 8
    .kernarg_segment_size: 72
    .language:       OpenCL C
    .language_version:
      - 2
      - 0
    .max_flat_workgroup_size: 1024
    .name:           _Z7k_finalPKfS0_S0_S0_S0_PKiS0_S0_Pf
    .private_segment_fixed_size: 0
    .sgpr_count:     24
    .sgpr_spill_count: 0
    .symbol:         _Z7k_finalPKfS0_S0_S0_S0_PKiS0_S0_Pf.kd
    .uniform_work_group_size: 1
    .uses_dynamic_stack: false
    .vgpr_count:     83
    .vgpr_spill_count: 0
    .wavefront_size: 64
